# MLA: fixed-shift fast softmax path (no max/sub; guarded, falls back to original online-softmax code), SWA wide stores via LDS staging, EpiRes loads hoisted
# speedup vs baseline: 1.0094x; 1.0052x over previous
.LBB0_1072:
	v_cmp_gt_u32_e64 s[4:5], 32, v192
	s_and_saveexec_b64 s[8:9], s[4:5]
	ds_write_b32 v187, v154 offset:128
	s_or_b64 exec, exec, s[8:9]
	v_add_u32_e32 v83, s28, v191
	ds_read_b128 v[78:81], v83 offset:128
	ds_read_b128 v[74:77], v83 offset:160
	s_ashr_i32 s20, s20, 8
	s_ashr_i32 s21, s20, 31
	s_lshl_b64 s[8:9], s[20:21], 24
	s_add_u32 s8, s24, s8
	s_addc_u32 s9, s25, s9
	s_lshl_b32 s21, s38, 17
	s_waitcnt lgkmcnt(1)
	v_rcp_f32_e32 v78, v78
	s_add_u32 s8, s8, s21
	ds_read_b128 v[70:73], v83 offset:192
	ds_read_b128 v[66:69], v83 offset:224
	s_addc_u32 s9, s9, 0
	s_lshl_b32 s21, s22, 7
	s_add_u32 s8, s8, s21
	v_and_b32_e32 v0, 1, v188
	s_addc_u32 s9, s9, 0
	v_cmp_eq_u32_e32 vcc, 0, v0
	v_lshl_or_b32 v0, v189, 12, v190
	v_readlane_b32 s99, v251, 5
	s_lshr_b32 s99, s99, 6
	s_lshl_b32 s99, s99, 12
	s_add_i32 s99, s99, 0x14000
	v_mbcnt_lo_u32_b32 v249, -1, 0
	v_mbcnt_hi_u32_b32 v249, -1, v249
	v_lshrrev_b32_e32 v252, 5, v249
	v_and_b32_e32 v249, 31, v249
	v_lshlrev_b32_e32 v249, 1, v249
	v_lshl_add_u32 v249, v252, 9, v249
	v_add_u32_e32 v249, s99, v249
	v_mul_f32_e32 v84, v50, v78
	s_and_b32 s9, s9, 0xffff
	v_lshlrev_b32_e32 v50, 1, v0
	v_mov_b32_dpp v85, v84 quad_perm:[1,0,3,2] row_mask:0xf bank_mask:0xf bound_ctrl:1
	s_and_saveexec_b64 s[22:23], vcc
	s_cbranch_execz .LBB0_1076
	v_cvt_pk_bf16_f32 v84, v84, v85
	ds_write_b32 v249, v84
.LBB0_1076:
	s_or_b64 exec, exec, s[22:23]
	v_mul_f32_e32 v34, v34, v78
	s_nop 1
	v_mov_b32_dpp v78, v34 quad_perm:[1,0,3,2] row_mask:0xf bank_mask:0xf bound_ctrl:1
	s_and_saveexec_b64 s[22:23], vcc
	s_cbranch_execz .LBB0_1078
	v_cvt_pk_bf16_f32 v34, v34, v78
	ds_write_b32 v249, v34 offset:64
.LBB0_1078:
	s_or_b64 exec, exec, s[22:23]
	v_rcp_f32_e32 v50, v79
	v_or_b32_e32 v34, 0x400, v0
	v_lshlrev_b32_e32 v34, 1, v34
	v_mul_f32_e32 v51, v51, v50
	s_nop 1
	v_mov_b32_dpp v78, v51 quad_perm:[1,0,3,2] row_mask:0xf bank_mask:0xf bound_ctrl:1
	s_and_saveexec_b64 s[22:23], vcc
	s_cbranch_execz .LBB0_1080
	v_cvt_pk_bf16_f32 v51, v51, v78
	ds_write_b32 v249, v51 offset:128
.LBB0_1080:
	s_or_b64 exec, exec, s[22:23]
	v_mul_f32_e32 v35, v35, v50
	s_nop 1
	v_mov_b32_dpp v50, v35 quad_perm:[1,0,3,2] row_mask:0xf bank_mask:0xf bound_ctrl:1
	s_and_saveexec_b64 s[22:23], vcc
	s_cbranch_execz .LBB0_1082
	v_cvt_pk_bf16_f32 v35, v35, v50
	ds_write_b32 v249, v35 offset:192
.LBB0_1082:
	s_or_b64 exec, exec, s[22:23]
	v_rcp_f32_e32 v35, v80
	v_or_b32_e32 v34, 0x800, v0
	v_lshlrev_b32_e32 v34, 1, v34
	v_mul_f32_e32 v50, v52, v35
	s_nop 1
	v_mov_b32_dpp v51, v50 quad_perm:[1,0,3,2] row_mask:0xf bank_mask:0xf bound_ctrl:1
	s_and_saveexec_b64 s[22:23], vcc
	s_cbranch_execz .LBB0_1084
	v_cvt_pk_bf16_f32 v50, v50, v51
	ds_write_b32 v249, v50 offset:256
.LBB0_1084:
	s_or_b64 exec, exec, s[22:23]
	v_mul_f32_e32 v35, v36, v35
	s_nop 1
	v_mov_b32_dpp v36, v35 quad_perm:[1,0,3,2] row_mask:0xf bank_mask:0xf bound_ctrl:1
	s_and_saveexec_b64 s[22:23], vcc
	s_cbranch_execz .LBB0_1086
	v_cvt_pk_bf16_f32 v35, v35, v36
	ds_write_b32 v249, v35 offset:320
.LBB0_1086:
	s_or_b64 exec, exec, s[22:23]
	v_rcp_f32_e32 v35, v81
	v_or_b32_e32 v34, 0xc00, v0
	v_lshlrev_b32_e32 v34, 1, v34
	v_mul_f32_e32 v36, v53, v35
	s_nop 1
	v_mov_b32_dpp v50, v36 quad_perm:[1,0,3,2] row_mask:0xf bank_mask:0xf bound_ctrl:1
	s_and_saveexec_b64 s[22:23], vcc
	s_cbranch_execz .LBB0_1088
	v_cvt_pk_bf16_f32 v36, v36, v50
	ds_write_b32 v249, v36 offset:384
.LBB0_1088:
	s_or_b64 exec, exec, s[22:23]
	v_mul_f32_e32 v35, v37, v35
	s_nop 1
	v_mov_b32_dpp v36, v35 quad_perm:[1,0,3,2] row_mask:0xf bank_mask:0xf bound_ctrl:1
	s_and_saveexec_b64 s[22:23], vcc
	s_cbranch_execz .LBB0_1090
	v_cvt_pk_bf16_f32 v35, v35, v36
	ds_write_b32 v249, v35 offset:448
.LBB0_1090:
	s_or_b64 exec, exec, s[22:23]
	s_waitcnt lgkmcnt(2)
	v_rcp_f32_e32 v35, v74
	v_or_b32_e32 v34, 0x2000, v0
	v_lshlrev_b32_e32 v34, 1, v34
	v_mul_f32_e32 v36, v54, v35
	s_nop 1
	v_mov_b32_dpp v37, v36 quad_perm:[1,0,3,2] row_mask:0xf bank_mask:0xf bound_ctrl:1
	s_and_saveexec_b64 s[22:23], vcc
	s_cbranch_execz .LBB0_1092
	v_cvt_pk_bf16_f32 v36, v36, v37
	ds_write_b32 v249, v36 offset:1024
.LBB0_1092:
	s_or_b64 exec, exec, s[22:23]
	v_mul_f32_e32 v35, v38, v35
	s_nop 1
	v_mov_b32_dpp v36, v35 quad_perm:[1,0,3,2] row_mask:0xf bank_mask:0xf bound_ctrl:1
	s_and_saveexec_b64 s[22:23], vcc
	s_cbranch_execz .LBB0_1094
	v_cvt_pk_bf16_f32 v35, v35, v36
	ds_write_b32 v249, v35 offset:1088
.LBB0_1094:
	s_or_b64 exec, exec, s[22:23]
	v_rcp_f32_e32 v35, v75
	v_or_b32_e32 v34, 0x2400, v0
	v_lshlrev_b32_e32 v34, 1, v34
	v_mul_f32_e32 v36, v55, v35
	s_nop 1
	v_mov_b32_dpp v37, v36 quad_perm:[1,0,3,2] row_mask:0xf bank_mask:0xf bound_ctrl:1
	s_and_saveexec_b64 s[22:23], vcc
	s_cbranch_execz .LBB0_1096
	v_cvt_pk_bf16_f32 v36, v36, v37
	ds_write_b32 v249, v36 offset:1152
.LBB0_1096:
	s_or_b64 exec, exec, s[22:23]
	v_mul_f32_e32 v35, v39, v35
	s_nop 1
	v_mov_b32_dpp v36, v35 quad_perm:[1,0,3,2] row_mask:0xf bank_mask:0xf bound_ctrl:1
	s_and_saveexec_b64 s[22:23], vcc
	s_cbranch_execz .LBB0_1098
	v_cvt_pk_bf16_f32 v35, v35, v36
	ds_write_b32 v249, v35 offset:1216
.LBB0_1098:
	s_or_b64 exec, exec, s[22:23]
	v_rcp_f32_e32 v35, v76
	v_or_b32_e32 v34, 0x2800, v0
	v_lshlrev_b32_e32 v34, 1, v34
	v_mul_f32_e32 v36, v56, v35
	s_nop 1
	v_mov_b32_dpp v37, v36 quad_perm:[1,0,3,2] row_mask:0xf bank_mask:0xf bound_ctrl:1
	s_and_saveexec_b64 s[22:23], vcc
	s_cbranch_execz .LBB0_1100
	v_cvt_pk_bf16_f32 v36, v36, v37
	ds_write_b32 v249, v36 offset:1280
.LBB0_1100:
	s_or_b64 exec, exec, s[22:23]
	v_mul_f32_e32 v35, v40, v35
	s_nop 1
	v_mov_b32_dpp v36, v35 quad_perm:[1,0,3,2] row_mask:0xf bank_mask:0xf bound_ctrl:1
	s_and_saveexec_b64 s[22:23], vcc
	s_cbranch_execz .LBB0_1102
	v_cvt_pk_bf16_f32 v35, v35, v36
	ds_write_b32 v249, v35 offset:1344
.LBB0_1102:
	s_or_b64 exec, exec, s[22:23]
	v_rcp_f32_e32 v35, v77
	v_or_b32_e32 v34, 0x2c00, v0
	v_lshlrev_b32_e32 v34, 1, v34
	v_mul_f32_e32 v36, v57, v35
	s_nop 1
	v_mov_b32_dpp v37, v36 quad_perm:[1,0,3,2] row_mask:0xf bank_mask:0xf bound_ctrl:1
	s_and_saveexec_b64 s[22:23], vcc
	s_cbranch_execz .LBB0_1104
	v_cvt_pk_bf16_f32 v36, v36, v37
	ds_write_b32 v249, v36 offset:1408
.LBB0_1104:
	s_or_b64 exec, exec, s[22:23]
	v_mul_f32_e32 v35, v41, v35
	s_nop 1
	v_mov_b32_dpp v36, v35 quad_perm:[1,0,3,2] row_mask:0xf bank_mask:0xf bound_ctrl:1
	s_and_saveexec_b64 s[22:23], vcc
	s_cbranch_execz .LBB0_1106
	v_cvt_pk_bf16_f32 v35, v35, v36
	ds_write_b32 v249, v35 offset:1472
.LBB0_1106:
	s_or_b64 exec, exec, s[22:23]
	s_waitcnt lgkmcnt(1)
	v_rcp_f32_e32 v35, v70
	v_or_b32_e32 v34, 0x4000, v0
	v_lshlrev_b32_e32 v34, 1, v34
	v_mul_f32_e32 v36, v58, v35
	s_nop 1
	v_mov_b32_dpp v37, v36 quad_perm:[1,0,3,2] row_mask:0xf bank_mask:0xf bound_ctrl:1
	s_and_saveexec_b64 s[22:23], vcc
	s_cbranch_execz .LBB0_1108
	v_cvt_pk_bf16_f32 v36, v36, v37
	ds_write_b32 v249, v36 offset:2048
.LBB0_1108:
	s_or_b64 exec, exec, s[22:23]
	v_mul_f32_e32 v35, v42, v35
	s_nop 1
	v_mov_b32_dpp v36, v35 quad_perm:[1,0,3,2] row_mask:0xf bank_mask:0xf bound_ctrl:1
	s_and_saveexec_b64 s[22:23], vcc
	s_cbranch_execz .LBB0_1110
	v_cvt_pk_bf16_f32 v35, v35, v36
	ds_write_b32 v249, v35 offset:2112
.LBB0_1110:
	s_or_b64 exec, exec, s[22:23]
	v_rcp_f32_e32 v35, v71
	v_or_b32_e32 v34, 0x4400, v0
	v_lshlrev_b32_e32 v34, 1, v34
	v_mul_f32_e32 v36, v59, v35
	s_nop 1
	v_mov_b32_dpp v37, v36 quad_perm:[1,0,3,2] row_mask:0xf bank_mask:0xf bound_ctrl:1
	s_and_saveexec_b64 s[22:23], vcc
	s_cbranch_execz .LBB0_1112
	v_cvt_pk_bf16_f32 v36, v36, v37
	ds_write_b32 v249, v36 offset:2176
.LBB0_1112:
	s_or_b64 exec, exec, s[22:23]
	v_mul_f32_e32 v35, v43, v35
	s_nop 1
	v_mov_b32_dpp v36, v35 quad_perm:[1,0,3,2] row_mask:0xf bank_mask:0xf bound_ctrl:1
	s_and_saveexec_b64 s[22:23], vcc
	s_cbranch_execz .LBB0_1114
	v_cvt_pk_bf16_f32 v35, v35, v36
	ds_write_b32 v249, v35 offset:2240
.LBB0_1114:
	s_or_b64 exec, exec, s[22:23]
	v_rcp_f32_e32 v35, v72
	v_or_b32_e32 v34, 0x4800, v0
	v_lshlrev_b32_e32 v34, 1, v34
	v_mul_f32_e32 v36, v60, v35
	s_nop 1
	v_mov_b32_dpp v37, v36 quad_perm:[1,0,3,2] row_mask:0xf bank_mask:0xf bound_ctrl:1
	s_and_saveexec_b64 s[22:23], vcc
	s_cbranch_execz .LBB0_1116
	v_cvt_pk_bf16_f32 v36, v36, v37
	ds_write_b32 v249, v36 offset:2304
.LBB0_1116:
	s_or_b64 exec, exec, s[22:23]
	v_mul_f32_e32 v35, v44, v35
	s_nop 1
	v_mov_b32_dpp v36, v35 quad_perm:[1,0,3,2] row_mask:0xf bank_mask:0xf bound_ctrl:1
	s_and_saveexec_b64 s[22:23], vcc
	s_cbranch_execz .LBB0_1118
	v_cvt_pk_bf16_f32 v35, v35, v36
	ds_write_b32 v249, v35 offset:2368
.LBB0_1118:
	s_or_b64 exec, exec, s[22:23]
	v_rcp_f32_e32 v35, v73
	v_or_b32_e32 v34, 0x4c00, v0
	v_lshlrev_b32_e32 v34, 1, v34
	v_mul_f32_e32 v36, v61, v35
	s_nop 1
	v_mov_b32_dpp v37, v36 quad_perm:[1,0,3,2] row_mask:0xf bank_mask:0xf bound_ctrl:1
	s_and_saveexec_b64 s[22:23], vcc
	s_cbranch_execz .LBB0_1120
	v_cvt_pk_bf16_f32 v36, v36, v37
	ds_write_b32 v249, v36 offset:2432
.LBB0_1120:
	s_or_b64 exec, exec, s[22:23]
	v_mul_f32_e32 v35, v45, v35
	s_nop 1
	v_mov_b32_dpp v36, v35 quad_perm:[1,0,3,2] row_mask:0xf bank_mask:0xf bound_ctrl:1
	s_and_saveexec_b64 s[22:23], vcc
	s_cbranch_execz .LBB0_1122
	v_cvt_pk_bf16_f32 v35, v35, v36
	ds_write_b32 v249, v35 offset:2496
.LBB0_1122:
	s_or_b64 exec, exec, s[22:23]
	s_waitcnt lgkmcnt(0)
	v_rcp_f32_e32 v35, v66
	v_or_b32_e32 v34, 0x6000, v0
	v_lshlrev_b32_e32 v34, 1, v34
	v_mul_f32_e32 v36, v62, v35
	s_nop 1
	v_mov_b32_dpp v37, v36 quad_perm:[1,0,3,2] row_mask:0xf bank_mask:0xf bound_ctrl:1
	s_and_saveexec_b64 s[22:23], vcc
	s_cbranch_execz .LBB0_1124
	v_cvt_pk_bf16_f32 v36, v36, v37
	ds_write_b32 v249, v36 offset:3072
.LBB0_1124:
	s_or_b64 exec, exec, s[22:23]
	v_mul_f32_e32 v35, v46, v35
	s_nop 1
	v_mov_b32_dpp v36, v35 quad_perm:[1,0,3,2] row_mask:0xf bank_mask:0xf bound_ctrl:1
	s_and_saveexec_b64 s[22:23], vcc
	s_cbranch_execz .LBB0_1126
	v_cvt_pk_bf16_f32 v35, v35, v36
	ds_write_b32 v249, v35 offset:3136
.LBB0_1126:
	s_or_b64 exec, exec, s[22:23]
	v_rcp_f32_e32 v35, v67
	v_or_b32_e32 v34, 0x6400, v0
	v_lshlrev_b32_e32 v34, 1, v34
	v_mul_f32_e32 v36, v63, v35
	s_nop 1
	v_mov_b32_dpp v37, v36 quad_perm:[1,0,3,2] row_mask:0xf bank_mask:0xf bound_ctrl:1
	s_and_saveexec_b64 s[22:23], vcc
	s_cbranch_execz .LBB0_1128
	v_cvt_pk_bf16_f32 v36, v36, v37
	ds_write_b32 v249, v36 offset:3200
.LBB0_1128:
	s_or_b64 exec, exec, s[22:23]
	v_mul_f32_e32 v35, v47, v35
	s_nop 1
	v_mov_b32_dpp v36, v35 quad_perm:[1,0,3,2] row_mask:0xf bank_mask:0xf bound_ctrl:1
	s_and_saveexec_b64 s[22:23], vcc
	s_cbranch_execz .LBB0_1130
	v_cvt_pk_bf16_f32 v35, v35, v36
	ds_write_b32 v249, v35 offset:3264
.LBB0_1130:
	s_or_b64 exec, exec, s[22:23]
	v_rcp_f32_e32 v35, v68
	v_or_b32_e32 v34, 0x6800, v0
	v_lshlrev_b32_e32 v34, 1, v34
	v_mul_f32_e32 v36, v64, v35
	s_nop 1
	v_mov_b32_dpp v37, v36 quad_perm:[1,0,3,2] row_mask:0xf bank_mask:0xf bound_ctrl:1
	s_and_saveexec_b64 s[22:23], vcc
	s_cbranch_execz .LBB0_1132
	v_cvt_pk_bf16_f32 v36, v36, v37
	ds_write_b32 v249, v36 offset:3328
.LBB0_1132:
	s_or_b64 exec, exec, s[22:23]
	v_mul_f32_e32 v35, v48, v35
	s_nop 1
	v_mov_b32_dpp v36, v35 quad_perm:[1,0,3,2] row_mask:0xf bank_mask:0xf bound_ctrl:1
	s_and_saveexec_b64 s[22:23], vcc
	s_cbranch_execz .LBB0_1134
	v_cvt_pk_bf16_f32 v35, v35, v36
	ds_write_b32 v249, v35 offset:3392
.LBB0_1134:
	s_or_b64 exec, exec, s[22:23]
	v_rcp_f32_e32 v35, v69
	v_or_b32_e32 v34, 0x6c00, v0
	v_lshlrev_b32_e32 v34, 1, v34
	v_mul_f32_e32 v36, v65, v35
	s_nop 1
	v_mov_b32_dpp v37, v36 quad_perm:[1,0,3,2] row_mask:0xf bank_mask:0xf bound_ctrl:1
	s_and_saveexec_b64 s[22:23], vcc
	s_cbranch_execz .LBB0_1136
	v_cvt_pk_bf16_f32 v36, v36, v37
	ds_write_b32 v249, v36 offset:3456
.LBB0_1136:
	s_or_b64 exec, exec, s[22:23]
	v_mul_f32_e32 v35, v49, v35
	s_nop 1
	v_mov_b32_dpp v36, v35 quad_perm:[1,0,3,2] row_mask:0xf bank_mask:0xf bound_ctrl:1
	s_and_saveexec_b64 s[22:23], vcc
	s_cbranch_execz .LBB0_1138
	v_cvt_pk_bf16_f32 v35, v35, v36
	ds_write_b32 v249, v35 offset:3520
.LBB0_1138:
	s_or_b64 exec, exec, s[22:23]
	s_waitcnt lgkmcnt(0)
	v_mbcnt_lo_u32_b32 v249, -1, 0
	v_mbcnt_hi_u32_b32 v249, -1, v249
	v_and_b32_e32 v252, 7, v249
	v_lshrrev_b32_e32 v249, 3, v249
	v_lshlrev_b32_e32 v252, 4, v252
	v_lshl_or_b32 v249, v249, 11, v252
	v_mbcnt_lo_u32_b32 v252, -1, 0
	v_mbcnt_hi_u32_b32 v252, -1, v252
	v_lshl_add_u32 v252, v252, 4, s99
	ds_read_b128 v[252:255], v252
	s_mov_b32 s100, 0x0
	s_waitcnt lgkmcnt(0)
	buffer_store_dwordx4 v[252:255], v249, s[8:11], s100 offen sc1
	s_nop 1
	v_mbcnt_lo_u32_b32 v252, -1, 0
	v_mbcnt_hi_u32_b32 v252, -1, v252
	v_lshl_add_u32 v252, v252, 4, s99
	ds_read_b128 v[252:255], v252 offset:1024
	s_mov_b32 s100, 0x4000
	s_waitcnt lgkmcnt(0)
	buffer_store_dwordx4 v[252:255], v249, s[8:11], s100 offen sc1
	s_nop 1
	v_mbcnt_lo_u32_b32 v252, -1, 0
	v_mbcnt_hi_u32_b32 v252, -1, v252
	v_lshl_add_u32 v252, v252, 4, s99
	ds_read_b128 v[252:255], v252 offset:2048
	s_mov_b32 s100, 0x8000
	s_waitcnt lgkmcnt(0)
	buffer_store_dwordx4 v[252:255], v249, s[8:11], s100 offen sc1
	s_nop 1
	v_mbcnt_lo_u32_b32 v252, -1, 0
	v_mbcnt_hi_u32_b32 v252, -1, v252
	v_lshl_add_u32 v252, v252, 4, s99
	ds_read_b128 v[252:255], v252 offset:3072
	s_mov_b32 s100, 0xc000
	s_waitcnt lgkmcnt(0)
	buffer_store_dwordx4 v[252:255], v249, s[8:11], s100 offen sc1
	s_nop 1
	v_mbcnt_lo_u32_b32 v249, -1, 0
	v_mbcnt_hi_u32_b32 v249, -1, v249
	v_lshrrev_b32_e32 v252, 5, v249
	v_and_b32_e32 v249, 31, v249
	v_lshlrev_b32_e32 v249, 1, v249
	v_lshl_add_u32 v249, v252, 9, v249
	v_add_u32_e32 v249, s99, v249
	s_waitcnt lgkmcnt(0)
	s_and_saveexec_b64 s[22:23], s[4:5]
	ds_write_b32 v187, v82 offset:128
	s_or_b64 exec, exec, s[22:23]
	ds_read_b128 v[46:49], v83 offset:128
	ds_read_b128 v[42:45], v83 offset:160
	ds_read_b128 v[38:41], v83 offset:192
	ds_read_b128 v[34:37], v83 offset:224
	v_or_b32_e32 v52, 0x8000, v0
	s_waitcnt lgkmcnt(3)
	v_rcp_f32_e32 v46, v46
	s_nop 0
	v_mul_f32_e32 v50, v18, v46
	s_nop 1
	v_mov_b32_dpp v51, v50 quad_perm:[1,0,3,2] row_mask:0xf bank_mask:0xf bound_ctrl:1
	v_lshlrev_b32_e32 v18, 1, v52
	s_and_saveexec_b64 s[4:5], vcc
	s_cbranch_execz .LBB0_1142
	v_cvt_pk_bf16_f32 v50, v50, v51
	ds_write_b32 v249, v50
.LBB0_1142:
	s_or_b64 exec, exec, s[4:5]
	v_mul_f32_e32 v2, v2, v46
	s_nop 1
	v_mov_b32_dpp v46, v2 quad_perm:[1,0,3,2] row_mask:0xf bank_mask:0xf bound_ctrl:1
	s_and_saveexec_b64 s[4:5], vcc
	s_cbranch_execz .LBB0_1144
	v_cvt_pk_bf16_f32 v2, v2, v46
	ds_write_b32 v249, v2 offset:64
.LBB0_1144:
	s_or_b64 exec, exec, s[4:5]
	v_rcp_f32_e32 v18, v47
	v_or_b32_e32 v2, 0x8400, v0
	v_lshlrev_b32_e32 v2, 1, v2
	v_mul_f32_e32 v19, v19, v18
	s_nop 1
	v_mov_b32_dpp v46, v19 quad_perm:[1,0,3,2] row_mask:0xf bank_mask:0xf bound_ctrl:1
	s_and_saveexec_b64 s[4:5], vcc
	s_cbranch_execz .LBB0_1146
	v_cvt_pk_bf16_f32 v19, v19, v46
	ds_write_b32 v249, v19 offset:128
.LBB0_1146:
	s_or_b64 exec, exec, s[4:5]
	v_mul_f32_e32 v3, v3, v18
	s_nop 1
	v_mov_b32_dpp v18, v3 quad_perm:[1,0,3,2] row_mask:0xf bank_mask:0xf bound_ctrl:1
	s_and_saveexec_b64 s[4:5], vcc
	s_cbranch_execz .LBB0_1148
	v_cvt_pk_bf16_f32 v3, v3, v18
	ds_write_b32 v249, v3 offset:192
.LBB0_1148:
	s_or_b64 exec, exec, s[4:5]
	v_rcp_f32_e32 v3, v48
	v_or_b32_e32 v2, 0x8800, v0
	v_lshlrev_b32_e32 v2, 1, v2
	v_mul_f32_e32 v18, v20, v3
	s_nop 1
	v_mov_b32_dpp v19, v18 quad_perm:[1,0,3,2] row_mask:0xf bank_mask:0xf bound_ctrl:1
	s_and_saveexec_b64 s[4:5], vcc
	s_cbranch_execz .LBB0_1150
	v_cvt_pk_bf16_f32 v18, v18, v19
	ds_write_b32 v249, v18 offset:256
.LBB0_1150:
	s_or_b64 exec, exec, s[4:5]
	v_mul_f32_e32 v3, v4, v3
	s_nop 1
	v_mov_b32_dpp v4, v3 quad_perm:[1,0,3,2] row_mask:0xf bank_mask:0xf bound_ctrl:1
	s_and_saveexec_b64 s[4:5], vcc
	s_cbranch_execz .LBB0_1152
	v_cvt_pk_bf16_f32 v3, v3, v4
	ds_write_b32 v249, v3 offset:320
.LBB0_1152:
	s_or_b64 exec, exec, s[4:5]
	v_rcp_f32_e32 v3, v49
	v_or_b32_e32 v2, 0x8c00, v0
	v_lshlrev_b32_e32 v2, 1, v2
	v_mul_f32_e32 v4, v21, v3
	s_nop 1
	v_mov_b32_dpp v18, v4 quad_perm:[1,0,3,2] row_mask:0xf bank_mask:0xf bound_ctrl:1
	s_and_saveexec_b64 s[4:5], vcc
	s_cbranch_execz .LBB0_1154
	v_cvt_pk_bf16_f32 v4, v4, v18
	ds_write_b32 v249, v4 offset:384
.LBB0_1154:
	s_or_b64 exec, exec, s[4:5]
	v_mul_f32_e32 v3, v5, v3
	s_nop 1
	v_mov_b32_dpp v4, v3 quad_perm:[1,0,3,2] row_mask:0xf bank_mask:0xf bound_ctrl:1
	s_and_saveexec_b64 s[4:5], vcc
	s_cbranch_execz .LBB0_1156
	v_cvt_pk_bf16_f32 v3, v3, v4
	ds_write_b32 v249, v3 offset:448
.LBB0_1156:
	s_or_b64 exec, exec, s[4:5]
	s_waitcnt lgkmcnt(2)
	v_rcp_f32_e32 v3, v42
	v_or_b32_e32 v2, 0xa000, v0
	v_lshlrev_b32_e32 v2, 1, v2
	v_mul_f32_e32 v4, v22, v3
	s_nop 1
	v_mov_b32_dpp v5, v4 quad_perm:[1,0,3,2] row_mask:0xf bank_mask:0xf bound_ctrl:1
	s_and_saveexec_b64 s[4:5], vcc
	s_cbranch_execz .LBB0_1158
	v_cvt_pk_bf16_f32 v4, v4, v5
	ds_write_b32 v249, v4 offset:1024
.LBB0_1158:
	s_or_b64 exec, exec, s[4:5]
	v_mul_f32_e32 v3, v6, v3
	s_nop 1
	v_mov_b32_dpp v4, v3 quad_perm:[1,0,3,2] row_mask:0xf bank_mask:0xf bound_ctrl:1
	s_and_saveexec_b64 s[4:5], vcc
	s_cbranch_execz .LBB0_1160
	v_cvt_pk_bf16_f32 v3, v3, v4
	ds_write_b32 v249, v3 offset:1088
.LBB0_1160:
	s_or_b64 exec, exec, s[4:5]
	v_rcp_f32_e32 v3, v43
	v_or_b32_e32 v2, 0xa400, v0
	v_lshlrev_b32_e32 v2, 1, v2
	v_mul_f32_e32 v4, v23, v3
	s_nop 1
	v_mov_b32_dpp v5, v4 quad_perm:[1,0,3,2] row_mask:0xf bank_mask:0xf bound_ctrl:1
	s_and_saveexec_b64 s[4:5], vcc
	s_cbranch_execz .LBB0_1162
	v_cvt_pk_bf16_f32 v4, v4, v5
	ds_write_b32 v249, v4 offset:1152
.LBB0_1162:
	s_or_b64 exec, exec, s[4:5]
	v_mul_f32_e32 v3, v7, v3
	s_nop 1
	v_mov_b32_dpp v4, v3 quad_perm:[1,0,3,2] row_mask:0xf bank_mask:0xf bound_ctrl:1
	s_and_saveexec_b64 s[4:5], vcc
	s_cbranch_execz .LBB0_1164
	v_cvt_pk_bf16_f32 v3, v3, v4
	ds_write_b32 v249, v3 offset:1216
.LBB0_1164:
	s_or_b64 exec, exec, s[4:5]
	v_rcp_f32_e32 v3, v44
	v_or_b32_e32 v2, 0xa800, v0
	v_lshlrev_b32_e32 v2, 1, v2
	v_mul_f32_e32 v4, v24, v3
	s_nop 1
	v_mov_b32_dpp v5, v4 quad_perm:[1,0,3,2] row_mask:0xf bank_mask:0xf bound_ctrl:1
	s_and_saveexec_b64 s[4:5], vcc
	s_cbranch_execz .LBB0_1166
	v_cvt_pk_bf16_f32 v4, v4, v5
	ds_write_b32 v249, v4 offset:1280
.LBB0_1166:
	s_or_b64 exec, exec, s[4:5]
	v_mul_f32_e32 v3, v8, v3
	s_nop 1
	v_mov_b32_dpp v4, v3 quad_perm:[1,0,3,2] row_mask:0xf bank_mask:0xf bound_ctrl:1
	s_and_saveexec_b64 s[4:5], vcc
	s_cbranch_execz .LBB0_1168
	v_cvt_pk_bf16_f32 v3, v3, v4
	ds_write_b32 v249, v3 offset:1344
.LBB0_1168:
	s_or_b64 exec, exec, s[4:5]
	v_rcp_f32_e32 v3, v45
	v_or_b32_e32 v2, 0xac00, v0
	v_lshlrev_b32_e32 v2, 1, v2
	v_mul_f32_e32 v4, v25, v3
	s_nop 1
	v_mov_b32_dpp v5, v4 quad_perm:[1,0,3,2] row_mask:0xf bank_mask:0xf bound_ctrl:1
	s_and_saveexec_b64 s[4:5], vcc
	s_cbranch_execz .LBB0_1170
	v_cvt_pk_bf16_f32 v4, v4, v5
	ds_write_b32 v249, v4 offset:1408
.LBB0_1170:
	s_or_b64 exec, exec, s[4:5]
	v_mul_f32_e32 v3, v9, v3
	s_nop 1
	v_mov_b32_dpp v4, v3 quad_perm:[1,0,3,2] row_mask:0xf bank_mask:0xf bound_ctrl:1
	s_and_saveexec_b64 s[4:5], vcc
	s_cbranch_execz .LBB0_1172
	v_cvt_pk_bf16_f32 v3, v3, v4
	ds_write_b32 v249, v3 offset:1472
.LBB0_1172:
	s_or_b64 exec, exec, s[4:5]
	s_waitcnt lgkmcnt(1)
	v_rcp_f32_e32 v3, v38
	v_or_b32_e32 v2, 0xc000, v0
	v_lshlrev_b32_e32 v2, 1, v2
	v_mul_f32_e32 v4, v26, v3
	s_nop 1
	v_mov_b32_dpp v5, v4 quad_perm:[1,0,3,2] row_mask:0xf bank_mask:0xf bound_ctrl:1
	s_and_saveexec_b64 s[4:5], vcc
	s_cbranch_execz .LBB0_1174
	v_cvt_pk_bf16_f32 v4, v4, v5
	ds_write_b32 v249, v4 offset:2048
.LBB0_1174:
	s_or_b64 exec, exec, s[4:5]
	v_mul_f32_e32 v3, v10, v3
	s_nop 1
	v_mov_b32_dpp v4, v3 quad_perm:[1,0,3,2] row_mask:0xf bank_mask:0xf bound_ctrl:1
	s_and_saveexec_b64 s[4:5], vcc
	s_cbranch_execz .LBB0_1176
	v_cvt_pk_bf16_f32 v3, v3, v4
	ds_write_b32 v249, v3 offset:2112
.LBB0_1176:
	s_or_b64 exec, exec, s[4:5]
	v_rcp_f32_e32 v3, v39
	v_or_b32_e32 v2, 0xc400, v0
	v_lshlrev_b32_e32 v2, 1, v2
	v_mul_f32_e32 v4, v27, v3
	s_nop 1
	v_mov_b32_dpp v5, v4 quad_perm:[1,0,3,2] row_mask:0xf bank_mask:0xf bound_ctrl:1
	s_and_saveexec_b64 s[4:5], vcc
	s_cbranch_execz .LBB0_1178
	v_cvt_pk_bf16_f32 v4, v4, v5
	ds_write_b32 v249, v4 offset:2176
.LBB0_1178:
	s_or_b64 exec, exec, s[4:5]
	v_mul_f32_e32 v3, v11, v3
	s_nop 1
	v_mov_b32_dpp v4, v3 quad_perm:[1,0,3,2] row_mask:0xf bank_mask:0xf bound_ctrl:1
	s_and_saveexec_b64 s[4:5], vcc
	s_cbranch_execz .LBB0_1180
	v_cvt_pk_bf16_f32 v3, v3, v4
	ds_write_b32 v249, v3 offset:2240
.LBB0_1180:
	s_or_b64 exec, exec, s[4:5]
	v_rcp_f32_e32 v3, v40
	v_or_b32_e32 v2, 0xc800, v0
	v_lshlrev_b32_e32 v2, 1, v2
	v_mul_f32_e32 v4, v28, v3
	s_nop 1
	v_mov_b32_dpp v5, v4 quad_perm:[1,0,3,2] row_mask:0xf bank_mask:0xf bound_ctrl:1
	s_and_saveexec_b64 s[4:5], vcc
	s_cbranch_execz .LBB0_1182
	v_cvt_pk_bf16_f32 v4, v4, v5
	ds_write_b32 v249, v4 offset:2304
.LBB0_1182:
	s_or_b64 exec, exec, s[4:5]
	v_mul_f32_e32 v3, v12, v3
	s_nop 1
	v_mov_b32_dpp v4, v3 quad_perm:[1,0,3,2] row_mask:0xf bank_mask:0xf bound_ctrl:1
	s_and_saveexec_b64 s[4:5], vcc
	s_cbranch_execz .LBB0_1184
	v_cvt_pk_bf16_f32 v3, v3, v4
	ds_write_b32 v249, v3 offset:2368
.LBB0_1184:
	s_or_b64 exec, exec, s[4:5]
	v_rcp_f32_e32 v3, v41
	v_or_b32_e32 v2, 0xcc00, v0
	v_lshlrev_b32_e32 v2, 1, v2
	v_mul_f32_e32 v4, v29, v3
	s_nop 1
	v_mov_b32_dpp v5, v4 quad_perm:[1,0,3,2] row_mask:0xf bank_mask:0xf bound_ctrl:1
	s_and_saveexec_b64 s[4:5], vcc
	s_cbranch_execz .LBB0_1186
	v_cvt_pk_bf16_f32 v4, v4, v5
	ds_write_b32 v249, v4 offset:2432
.LBB0_1186:
	s_or_b64 exec, exec, s[4:5]
	v_mul_f32_e32 v3, v13, v3
	s_nop 1
	v_mov_b32_dpp v4, v3 quad_perm:[1,0,3,2] row_mask:0xf bank_mask:0xf bound_ctrl:1
	s_and_saveexec_b64 s[4:5], vcc
	s_cbranch_execz .LBB0_1188
	v_cvt_pk_bf16_f32 v3, v3, v4
	ds_write_b32 v249, v3 offset:2496
.LBB0_1188:
	s_or_b64 exec, exec, s[4:5]
	s_waitcnt lgkmcnt(0)
	v_rcp_f32_e32 v3, v34
	v_or_b32_e32 v2, 0xe000, v0
	v_lshlrev_b32_e32 v2, 1, v2
	v_mul_f32_e32 v4, v30, v3
	s_nop 1
	v_mov_b32_dpp v5, v4 quad_perm:[1,0,3,2] row_mask:0xf bank_mask:0xf bound_ctrl:1
	s_and_saveexec_b64 s[4:5], vcc
	s_cbranch_execz .LBB0_1190
	v_cvt_pk_bf16_f32 v4, v4, v5
	ds_write_b32 v249, v4 offset:3072
.LBB0_1190:
	s_or_b64 exec, exec, s[4:5]
	v_mul_f32_e32 v3, v14, v3
	s_nop 1
	v_mov_b32_dpp v4, v3 quad_perm:[1,0,3,2] row_mask:0xf bank_mask:0xf bound_ctrl:1
	s_and_saveexec_b64 s[4:5], vcc
	s_cbranch_execz .LBB0_1192
	v_cvt_pk_bf16_f32 v3, v3, v4
	ds_write_b32 v249, v3 offset:3136
.LBB0_1192:
	s_or_b64 exec, exec, s[4:5]
	v_rcp_f32_e32 v3, v35
	v_or_b32_e32 v2, 0xe400, v0
	v_lshlrev_b32_e32 v2, 1, v2
	v_mul_f32_e32 v4, v31, v3
	s_nop 1
	v_mov_b32_dpp v5, v4 quad_perm:[1,0,3,2] row_mask:0xf bank_mask:0xf bound_ctrl:1
	s_and_saveexec_b64 s[4:5], vcc
	s_cbranch_execz .LBB0_1194
	v_cvt_pk_bf16_f32 v4, v4, v5
	ds_write_b32 v249, v4 offset:3200
.LBB0_1194:
	s_or_b64 exec, exec, s[4:5]
	v_mul_f32_e32 v3, v15, v3
	s_nop 1
	v_mov_b32_dpp v4, v3 quad_perm:[1,0,3,2] row_mask:0xf bank_mask:0xf bound_ctrl:1
	s_and_saveexec_b64 s[4:5], vcc
	s_cbranch_execz .LBB0_1196
	v_cvt_pk_bf16_f32 v3, v3, v4
	ds_write_b32 v249, v3 offset:3264
.LBB0_1196:
	s_or_b64 exec, exec, s[4:5]
	v_rcp_f32_e32 v3, v36
	v_or_b32_e32 v2, 0xe800, v0
	v_lshlrev_b32_e32 v2, 1, v2
	v_mul_f32_e32 v4, v32, v3
	s_nop 1
	v_mov_b32_dpp v5, v4 quad_perm:[1,0,3,2] row_mask:0xf bank_mask:0xf bound_ctrl:1
	s_and_saveexec_b64 s[4:5], vcc
	s_cbranch_execz .LBB0_1198
	v_cvt_pk_bf16_f32 v4, v4, v5
	ds_write_b32 v249, v4 offset:3328
.LBB0_1198:
	s_or_b64 exec, exec, s[4:5]
	v_mul_f32_e32 v3, v16, v3
	s_nop 1
	v_mov_b32_dpp v4, v3 quad_perm:[1,0,3,2] row_mask:0xf bank_mask:0xf bound_ctrl:1
	s_and_saveexec_b64 s[4:5], vcc
	s_cbranch_execz .LBB0_1200
	v_cvt_pk_bf16_f32 v3, v3, v4
	ds_write_b32 v249, v3 offset:3392
.LBB0_1200:
	s_or_b64 exec, exec, s[4:5]
	v_rcp_f32_e32 v2, v37
	v_or_b32_e32 v0, 0xec00, v0
	v_lshlrev_b32_e32 v0, 1, v0
	v_mul_f32_e32 v3, v33, v2
	s_nop 1
	v_mov_b32_dpp v4, v3 quad_perm:[1,0,3,2] row_mask:0xf bank_mask:0xf bound_ctrl:1
	s_and_saveexec_b64 s[4:5], vcc
	s_cbranch_execz .LBB0_1202
	v_cvt_pk_bf16_f32 v3, v3, v4
	ds_write_b32 v249, v3 offset:3456
.LBB0_1202:
	s_or_b64 exec, exec, s[4:5]
	v_mul_f32_e32 v2, v17, v2
	s_nop 1
	v_mov_b32_dpp v3, v2 quad_perm:[1,0,3,2] row_mask:0xf bank_mask:0xf bound_ctrl:1
	s_and_saveexec_b64 s[4:5], vcc
	s_cbranch_execz .LBB0_1204
	v_cvt_pk_bf16_f32 v2, v2, v3
	ds_write_b32 v249, v2 offset:3520
.LBB0_1204:
	s_or_b64 exec, exec, s[4:5]
	s_waitcnt lgkmcnt(0)
	v_mbcnt_lo_u32_b32 v249, -1, 0
	v_mbcnt_hi_u32_b32 v249, -1, v249
	v_and_b32_e32 v252, 7, v249
	v_lshrrev_b32_e32 v249, 3, v249
	v_lshlrev_b32_e32 v252, 4, v252
	v_lshl_or_b32 v249, v249, 11, v252
	v_mbcnt_lo_u32_b32 v252, -1, 0
	v_mbcnt_hi_u32_b32 v252, -1, v252
	v_lshl_add_u32 v252, v252, 4, s99
	ds_read_b128 v[252:255], v252
	s_mov_b32 s100, 0x10000
	s_waitcnt lgkmcnt(0)
	buffer_store_dwordx4 v[252:255], v249, s[8:11], s100 offen sc1
	s_nop 1
	v_mbcnt_lo_u32_b32 v252, -1, 0
	v_mbcnt_hi_u32_b32 v252, -1, v252
	v_lshl_add_u32 v252, v252, 4, s99
	ds_read_b128 v[252:255], v252 offset:1024
	s_mov_b32 s100, 0x14000
	s_waitcnt lgkmcnt(0)
	buffer_store_dwordx4 v[252:255], v249, s[8:11], s100 offen sc1
	s_nop 1
	v_mbcnt_lo_u32_b32 v252, -1, 0
	v_mbcnt_hi_u32_b32 v252, -1, v252
	v_lshl_add_u32 v252, v252, 4, s99
	ds_read_b128 v[252:255], v252 offset:2048
	s_mov_b32 s100, 0x18000
	s_waitcnt lgkmcnt(0)
	buffer_store_dwordx4 v[252:255], v249, s[8:11], s100 offen sc1
	s_nop 1
	v_mbcnt_lo_u32_b32 v252, -1, 0
	v_mbcnt_hi_u32_b32 v252, -1, v252
	v_lshl_add_u32 v252, v252, 4, s99
	ds_read_b128 v[252:255], v252 offset:3072
	s_mov_b32 s100, 0x1c000
	s_waitcnt lgkmcnt(0)
	buffer_store_dwordx4 v[252:255], v249, s[8:11], s100 offen sc1
	s_nop 1
	s_waitcnt lgkmcnt(0)
	s_waitcnt vmcnt(0)
	s_waitcnt vmcnt(63) expcnt(7) lgkmcnt(15)
	s_barrier
	s_and_saveexec_b64 s[4:5], s[2:3]
	s_cbranch_execz .LBB0_1042
	s_mov_b64 s[8:9], exec
	v_mbcnt_lo_u32_b32 v0, s8, 0
	v_mbcnt_hi_u32_b32 v0, s9, v0
	v_cmp_eq_u32_e32 vcc, 0, v0
	s_and_b64 s[22:23], exec, vcc
	s_mov_b64 exec, s[22:23]
	s_cbranch_execz .LBB0_1042
	s_lshl_b32 s21, s38, 2
	s_lshl_b32 s20, s20, 9
	s_and_b32 s21, s21, 0x1f0
	s_or_b32 s20, s20, s21
	s_addk_i32 s20, 0xc00
	s_ashr_i32 s21, s20, 31
	s_lshl_b64 s[20:21], s[20:21], 2
	s_add_u32 s20, s29, s20
	s_addc_u32 s21, s30, s21
	s_bcnt1_i32_b64 s8, s[8:9]
	v_mov_b32_e32 v0, s8
	global_atomic_add v1, v0, s[20:21]
	s_branch .LBB0_1042

.LBB0_1224:
	v_mov_b32_e32 v0, v181
	v_readlane_b32 s8, v251, 6
	v_mbcnt_lo_u32_b32 v0, -1, v0
	v_mbcnt_hi_u32_b32 v203, -1, v0
	v_and_b32_e32 v205, 63, v203
	v_or_b32_e32 v0, s8, v205
	v_mul_hi_i32 v1, v0, s30
	v_lshrrev_b32_e32 v2, 31, v1
	v_ashrrev_i32_e32 v1, 2, v1
	v_add_u32_e32 v2, v1, v2
	v_mad_u64_u32 v[4:5], s[8:9], v2, s91, v[0:1]
	v_lshrrev_b32_e32 v1, 1, v2
	v_xor_b32_e32 v1, v1, v203
	v_bfi_b32 v1, -8, v4, v1
	v_cmp_lt_i32_e32 vcc, 15, v1
	v_ashrrev_i32_e32 v3, 31, v2
	v_lshlrev_b32_e32 v4, 3, v1
	s_and_saveexec_b64 s[8:9], vcc
	s_xor_b64 s[8:9], exec, s[8:9]
	v_lshlrev_b64 v[2:3], 7, v[2:3]
	v_lshl_add_u64 v[2:3], s[50:51], 0, v[2:3]
	v_add_u32_e32 v180, 0xffffff80, v4
	v_lshl_add_u64 v[16:17], v[180:181], 1, v[2:3]
	s_or_saveexec_b64 s[8:9], s[8:9]
	v_mov_b64_e32 v[18:19], 0x1000
	s_xor_b64 exec, exec, s[8:9]
	v_lshlrev_b64 v[2:3], 8, v[2:3]
	v_lshl_add_u64 v[2:3], s[48:49], 0, v[2:3]
	v_ashrrev_i32_e32 v5, 31, v4
	v_lshl_add_u64 v[16:17], v[4:5], 1, v[2:3]
	v_mov_b64_e32 v[18:19], 0x2000
	s_or_b64 exec, exec, s[8:9]
	v_add_u32_e32 v4, 0x200, v0
	v_mul_hi_i32 v1, v4, s30
	v_lshrrev_b32_e32 v2, 31, v1
	v_ashrrev_i32_e32 v1, 2, v1
	v_add_u32_e32 v2, v1, v2
	v_lshrrev_b32_e32 v1, 1, v2
	v_mad_u64_u32 v[4:5], s[8:9], v2, s91, v[4:5]
	v_xor_b32_e32 v1, v1, v203
	v_bfi_b32 v1, -8, v4, v1
	v_cmp_lt_i32_e32 vcc, 15, v1
	v_ashrrev_i32_e32 v3, 31, v2
	v_lshlrev_b32_e32 v4, 3, v1
	s_and_saveexec_b64 s[8:9], vcc
	s_xor_b64 s[8:9], exec, s[8:9]
	v_lshlrev_b64 v[2:3], 7, v[2:3]
	v_lshl_add_u64 v[2:3], s[50:51], 0, v[2:3]
	v_add_u32_e32 v180, 0xffffff80, v4
	v_lshl_add_u64 v[20:21], v[180:181], 1, v[2:3]
	s_or_saveexec_b64 s[8:9], s[8:9]
	v_mov_b64_e32 v[22:23], 0x1000
	s_xor_b64 exec, exec, s[8:9]
	v_lshlrev_b64 v[2:3], 8, v[2:3]
	v_lshl_add_u64 v[2:3], s[48:49], 0, v[2:3]
	v_ashrrev_i32_e32 v5, 31, v4
	v_lshl_add_u64 v[20:21], v[4:5], 1, v[2:3]
	v_mov_b64_e32 v[22:23], 0x2000
	s_or_b64 exec, exec, s[8:9]
	v_add_u32_e32 v2, 0x400, v0
	v_mul_hi_i32 v0, v2, s30
	v_lshrrev_b32_e32 v1, 31, v0
	v_ashrrev_i32_e32 v0, 2, v0
	v_add_u32_e32 v0, v0, v1
	v_lshrrev_b32_e32 v1, 1, v0
	v_mad_u64_u32 v[2:3], s[8:9], v0, s91, v[2:3]
	v_xor_b32_e32 v1, v1, v203
	v_bfi_b32 v2, -8, v2, v1
	v_cmp_lt_i32_e32 vcc, 15, v2
	v_ashrrev_i32_e32 v1, 31, v0
	v_lshlrev_b32_e32 v2, 3, v2
	s_and_saveexec_b64 s[8:9], vcc
	s_xor_b64 s[8:9], exec, s[8:9]
	v_lshlrev_b64 v[0:1], 7, v[0:1]
	v_lshl_add_u64 v[0:1], s[50:51], 0, v[0:1]
	v_add_u32_e32 v180, 0xffffff80, v2
	v_lshl_add_u64 v[24:25], v[180:181], 1, v[0:1]
	s_or_saveexec_b64 s[8:9], s[8:9]
	v_mov_b64_e32 v[26:27], 0x1000
	s_xor_b64 exec, exec, s[8:9]
	v_lshlrev_b64 v[0:1], 8, v[0:1]
	v_lshl_add_u64 v[0:1], s[48:49], 0, v[0:1]
	v_ashrrev_i32_e32 v3, 31, v2
	v_lshl_add_u64 v[24:25], v[2:3], 1, v[0:1]
	v_mov_b64_e32 v[26:27], 0x2000
	s_or_b64 exec, exec, s[8:9]
	s_xor_b64 s[58:59], s[4:5], -1
	s_xor_b64 s[60:61], s[6:7], -1
	s_and_b64 s[4:5], s[4:5], exec
	s_cselect_b32 s57, s79, s70
	s_lshl_b32 s21, s57, 8
	s_add_i32 s44, s21, s26
	s_add_u32 s66, s46, s44
	s_mov_b32 s4, s45
	s_mov_b32 s5, s45
	s_addc_u32 s67, s47, 0
	s_mov_b32 s6, s45
	s_mov_b32 s7, s45
	s_mov_b32 s8, s45
	s_mov_b32 s9, s45
	s_mov_b32 s10, s45
	s_mov_b32 s11, s45
	s_mov_b32 s12, s45
	s_mov_b32 s13, s45
	s_mov_b32 s14, s45
	s_mov_b32 s15, s45
	s_mov_b32 s16, s45
	s_mov_b32 s17, s45
	s_mov_b32 s18, s45
	s_mov_b32 s19, s45
	v_mov_b64_e32 v[0:1], s[4:5]
	v_mov_b64_e32 v[2:3], s[6:7]
	v_mov_b64_e32 v[4:5], s[8:9]
	v_mov_b64_e32 v[6:7], s[10:11]
	v_mov_b64_e32 v[8:9], s[12:13]
	v_mov_b64_e32 v[10:11], s[14:15]
	v_mov_b64_e32 v[12:13], s[16:17]
	v_mov_b64_e32 v[14:15], s[18:19]
	s_lshl_b64 s[4:5], s[66:67], 9
	v_readlane_b32 s6, v251, 38
	s_add_u32 s8, s6, s4
	v_readlane_b32 s4, v251, 39
	s_addc_u32 s9, s4, s5
	s_lshl_b64 s[4:5], s[66:67], 4
	v_readlane_b32 s6, v251, 43
	s_add_u32 s6, s6, s4
	v_readlane_b32 s4, v251, 45
	s_addc_u32 s7, s4, s5
	s_lshl_b64 s[4:5], s[44:45], 8
	v_readlane_b32 s10, v251, 47
	s_mov_b32 m0, s88
	s_add_u32 s4, s10, s4
	v_readlane_b32 s10, v251, 48
	s_addc_u32 s5, s10, s5
	global_load_lds_dwordx4 v[16:17], off
	v_lshlrev_b32_e32 v180, 1, v18
	s_add_i32 m0, s88, 0x2000
	v_lshrrev_b32_e32 v204, 5, v205
	v_readlane_b32 s10, v251, 63
	v_and_b32_e32 v200, 31, v203
	s_waitcnt vmcnt(0)
	v_lshl_add_u64 v[126:127], v[16:17], 0, v[180:181]
	global_load_lds_dwordx4 v[20:21], off
	s_mov_b32 m0, s86
	v_or_b32_e32 v16, s10, v204
	v_lshlrev_b32_e32 v184, 1, v22
	v_mov_b32_e32 v185, v181
	global_load_lds_dwordx4 v[24:25], off
	s_mov_b32 m0, s27
	v_bitop3_b32 v18, v16, v200, 9 bitop3:0x6c
	v_and_or_b32 v16, v16, 17, s96
	v_mov_b32_e32 v17, v181
	v_lshl_add_u64 v[188:189], v[20:21], 0, v[184:185]
	v_lshlrev_b32_e32 v186, 1, v26
	v_mov_b32_e32 v187, v181
	global_load_lds_dwordx4 v[126:127], off
	s_mov_b32 m0, s38
	v_lshlrev_b64 v[16:17], 9, v[16:17]
	v_lshl_add_u64 v[120:121], v[24:25], 0, v[186:187]
	global_load_lds_dwordx4 v[188:189], off
	s_mov_b32 m0, s39
	v_lshl_add_u64 v[16:17], s[34:35], 0, v[16:17]
	v_lshlrev_b32_e32 v18, 4, v18
	v_mov_b32_e32 v19, v181
	v_readlane_b32 s10, v250, 27
	global_load_lds_dwordx4 v[120:121], off
	v_lshl_add_u64 v[16:17], v[16:17], 0, v[18:19]
	s_mov_b32 m0, s10
	v_readlane_b32 s10, v251, 57
	global_load_lds_dwordx4 v[16:17], off
	s_nop 0
	v_or_b32_e32 v16, s10, v204
	v_bitop3_b32 v18, v16, v200, 11 bitop3:0x6c
	v_and_or_b32 v16, v16, 19, s96
	v_mov_b32_e32 v17, v181
	v_lshlrev_b64 v[16:17], 9, v[16:17]
	v_lshl_add_u64 v[16:17], s[34:35], 0, v[16:17]
	v_lshlrev_b32_e32 v18, 4, v18
	v_lshl_add_u64 v[16:17], v[16:17], 0, v[18:19]
	s_mov_b32 m0, s74
	v_readlane_b32 s10, v251, 61
	global_load_lds_dwordx4 v[16:17], off
	s_nop 0
	v_or_b32_e32 v16, s10, v204
	v_bitop3_b32 v18, v16, v200, 13 bitop3:0x6c
	v_and_or_b32 v16, v16, 17, s82
	v_mov_b32_e32 v17, v181
	v_lshlrev_b64 v[16:17], 9, v[16:17]
	v_lshl_add_u64 v[16:17], s[34:35], 0, v[16:17]
	v_lshlrev_b32_e32 v18, 4, v18
	v_lshl_add_u64 v[16:17], v[16:17], 0, v[18:19]
	s_mov_b32 m0, s76
	v_readlane_b32 s10, v250, 0
	global_load_lds_dwordx4 v[16:17], off
	s_nop 0
	v_or_b32_e32 v16, s10, v204
	v_bitop3_b32 v18, v16, v200, 15 bitop3:0x6c
	v_and_or_b32 v16, v16, 19, s82
	v_mov_b32_e32 v17, v181
	v_lshlrev_b64 v[16:17], 9, v[16:17]
	v_lshl_add_u64 v[16:17], s[34:35], 0, v[16:17]
	v_lshlrev_b32_e32 v18, 4, v18
	v_lshl_add_u64 v[16:17], v[16:17], 0, v[18:19]
	s_mov_b32 m0, s78
	v_readlane_b32 s10, v250, 6
	global_load_lds_dwordx4 v[16:17], off
	s_nop 0
	v_or_b32_e32 v16, s10, v204
	v_bitop3_b32 v18, v16, v200, 9 bitop3:0x6c
	v_and_or_b32 v16, v16, 17, s84
	v_mov_b32_e32 v17, v181
	v_lshlrev_b64 v[16:17], 9, v[16:17]
	v_lshl_add_u64 v[16:17], s[34:35], 0, v[16:17]
	v_lshlrev_b32_e32 v18, 4, v18
	v_lshl_add_u64 v[16:17], v[16:17], 0, v[18:19]
	s_mov_b32 m0, s94
	v_readlane_b32 s10, v250, 9
	global_load_lds_dwordx4 v[16:17], off
	s_nop 0
	v_or_b32_e32 v16, s10, v204
	v_bitop3_b32 v18, v16, v200, 11 bitop3:0x6c
	v_and_or_b32 v16, v16, 19, s36
	v_mov_b32_e32 v17, v181
	v_lshlrev_b64 v[16:17], 9, v[16:17]
	v_lshl_add_u64 v[16:17], s[34:35], 0, v[16:17]
	v_lshlrev_b32_e32 v18, 4, v18
	v_lshl_add_u64 v[16:17], v[16:17], 0, v[18:19]
	s_mov_b32 m0, s24
	v_lshlrev_b32_e32 v20, 9, v200
	global_load_lds_dwordx4 v[16:17], off
	v_or_b32_e32 v16, s73, v204
	v_bitop3_b32 v18, v16, v200, 13 bitop3:0x6c
	v_and_or_b32 v16, v16, 17, s37
	v_mov_b32_e32 v17, v181
	v_lshlrev_b64 v[16:17], 9, v[16:17]
	v_lshl_add_u64 v[16:17], s[34:35], 0, v[16:17]
	v_lshlrev_b32_e32 v18, 4, v18
	v_lshl_add_u64 v[16:17], v[16:17], 0, v[18:19]
	s_mov_b32 m0, s28
	v_mov_b32_e32 v21, v181
	global_load_lds_dwordx4 v[16:17], off
	v_or_b32_e32 v16, s72, v204
	v_bitop3_b32 v18, v16, v200, 15 bitop3:0x6c
	v_and_or_b32 v16, v16, 19, s85
	v_mov_b32_e32 v17, v181
	v_lshlrev_b64 v[16:17], 9, v[16:17]
	v_lshl_add_u64 v[16:17], s[34:35], 0, v[16:17]
	v_lshlrev_b32_e32 v18, 4, v18
	v_lshl_add_u64 v[16:17], v[16:17], 0, v[18:19]
	s_mov_b32 m0, s90
	v_lshlrev_b32_e32 v18, 8, v204
	global_load_lds_dwordx4 v[16:17], off
	v_or_b32_e32 v16, s97, v204
	v_bitop3_b32 v26, v16, v200, 9 bitop3:0x6c
	v_and_or_b32 v16, v16, 17, s83
	v_mov_b32_e32 v17, v181
	v_lshlrev_b64 v[22:23], 9, v[16:17]
	v_lshl_add_u64 v[16:17], s[8:9], 0, v[20:21]
	v_lshl_add_u64 v[24:25], v[16:17], 0, v[18:19]
	global_load_dwordx4 v[16:19], v[24:25], off
	global_load_dwordx4 v[172:175], v[24:25], off offset:16
	v_lshl_add_u64 v[22:23], s[34:35], 0, v[22:23]
	v_lshlrev_b32_e32 v26, 4, v26
	v_mov_b32_e32 v27, v181
	v_lshl_add_u64 v[22:23], v[22:23], 0, v[26:27]
	s_mov_b32 m0, s31
	v_or_b32_e32 v21, s41, v204
	global_load_lds_dwordx4 v[22:23], off
	v_and_or_b32 v22, v21, 19, s92
	v_mov_b32_e32 v23, v181
	v_bitop3_b32 v26, v21, v200, 11 bitop3:0x6c
	v_lshlrev_b64 v[22:23], 9, v[22:23]
	v_lshl_add_u64 v[22:23], s[34:35], 0, v[22:23]
	v_lshlrev_b32_e32 v26, 4, v26
	v_lshl_add_u64 v[22:23], v[22:23], 0, v[26:27]
	s_mov_b32 m0, s42
	v_or_b32_e32 v21, s75, v204
	global_load_lds_dwordx4 v[22:23], off
	v_and_or_b32 v22, v21, 17, s93
	v_mov_b32_e32 v23, v181
	v_bitop3_b32 v26, v21, v200, 13 bitop3:0x6c
	v_lshlrev_b64 v[22:23], 9, v[22:23]
	v_lshl_add_u64 v[22:23], s[34:35], 0, v[22:23]
	v_lshlrev_b32_e32 v26, 4, v26
	v_lshl_add_u64 v[22:23], v[22:23], 0, v[26:27]
	s_mov_b32 m0, s87
	v_or_b32_e32 v21, s77, v204
	global_load_lds_dwordx4 v[22:23], off
	v_and_or_b32 v22, v21, 19, s95
	v_mov_b32_e32 v23, v181
	v_bitop3_b32 v26, v21, v200, 15 bitop3:0x6c
	v_lshlrev_b64 v[22:23], 9, v[22:23]
	v_lshl_add_u64 v[22:23], s[34:35], 0, v[22:23]
	v_lshlrev_b32_e32 v26, 4, v26
	v_lshl_add_u64 v[22:23], v[22:23], 0, v[26:27]
	s_mov_b32 m0, s71
	v_lshlrev_b32_e32 v21, 4, v200
	global_load_lds_dwordx4 v[22:23], off
	global_load_dwordx4 v[168:171], v[24:25], off offset:32
	global_load_dwordx4 v[112:115], v[24:25], off offset:48
	global_load_dwordx4 v[116:119], v[24:25], off offset:64
	global_load_dwordx4 v[122:125], v[24:25], off offset:80
	global_load_dwordx4 v[164:167], v[24:25], off offset:96
	global_load_dwordx4 v[160:163], v[24:25], off offset:112
	global_load_dwordx4 v[156:159], v[24:25], off offset:128
	global_load_dwordx4 v[152:155], v[24:25], off offset:144
	global_load_dwordx4 v[148:151], v[24:25], off offset:160
	global_load_dwordx4 v[128:131], v[24:25], off offset:176
	global_load_dwordx4 v[144:147], v[24:25], off offset:192
	global_load_dwordx4 v[140:143], v[24:25], off offset:208
	global_load_dwordx4 v[132:135], v[24:25], off offset:224
	global_load_dwordx4 v[136:139], v[24:25], off offset:240
	v_lshlrev_b32_e32 v23, 4, v204
	v_and_b32_e32 v201, 15, v203
	global_load_dwordx4 v[176:179], v21, s[6:7]
	v_or_b32_e32 v21, v23, v201
	v_add_u32_e32 v22, 0, v20
	v_lshlrev_b32_e32 v21, 4, v21
	v_add_u32_e32 v24, v22, v21
	s_waitcnt vmcnt(0)
	s_waitcnt vmcnt(0) lgkmcnt(0)
	s_barrier
	ds_read_b128 v[24:27], v24 offset:49152
	v_add_u32_e32 v28, 0x10000, v22
	s_waitcnt lgkmcnt(0)
	v_mfma_f32_32x32x16_bf16 v[64:79], v[24:27], v[16:19], 0
	v_add_u32_e32 v24, v28, v21
	ds_read_b128 v[24:27], v24
	v_add_u32_e32 v221, s43, v20
	v_add_u32_e32 v218, 0x20400, v22
	v_readlane_b32 s6, v251, 6
	s_lshl_b32 s9, s57, 2
	s_add_i32 s9, s9, 4
	s_waitcnt lgkmcnt(0)
	v_mfma_f32_32x32x16_bf16 v[48:63], v[24:27], v[16:19], 0
	v_bitop3_b32 v24, v23, v201, 1 bitop3:0x36
	v_lshlrev_b32_e32 v202, 4, v24
	v_add_u32_e32 v24, v22, v202
	ds_read_b128 v[24:27], v24 offset:49152
	v_add_u32_e32 v222, v221, v202
	s_ashr_i32 s11, s89, 31
	s_mov_b32 s10, 3
	s_waitcnt lgkmcnt(0)
	v_mfma_f32_32x32x16_bf16 v[64:79], v[24:27], v[172:175], v[64:79]
	v_add_u32_e32 v24, v28, v202
	ds_read_b128 v[24:27], v24
	ds_read_b128 v[222:225], v222
	s_waitcnt lgkmcnt(1)
	v_mfma_f32_32x32x16_bf16 v[48:63], v[24:27], v[172:175], v[48:63]
	v_bitop3_b32 v24, v23, v201, 2 bitop3:0x36
	v_lshlrev_b32_e32 v220, 4, v24
	v_add_u32_e32 v24, v22, v220
	ds_read_b128 v[24:27], v24 offset:49152
	s_waitcnt lgkmcnt(0)
	v_mfma_f32_32x32x16_bf16 v[64:79], v[24:27], v[168:171], v[64:79]
	v_add_u32_e32 v24, v28, v220
	ds_read_b128 v[24:27], v24
	s_waitcnt lgkmcnt(0)
	v_mfma_f32_32x32x16_bf16 v[48:63], v[24:27], v[168:171], v[48:63]
	v_bitop3_b32 v24, v23, v201, 3 bitop3:0x36
	v_lshlrev_b32_e32 v219, 4, v24
	v_add_u32_e32 v24, v22, v219
	ds_read_b128 v[24:27], v24 offset:49152
	s_waitcnt lgkmcnt(0)
	v_mfma_f32_32x32x16_bf16 v[64:79], v[24:27], v[112:115], v[64:79]
	v_add_u32_e32 v24, v28, v219
	ds_read_b128 v[24:27], v24
	s_waitcnt lgkmcnt(0)
	v_mfma_f32_32x32x16_bf16 v[48:63], v[24:27], v[112:115], v[48:63]
	v_bitop3_b32 v24, v23, v201, 4 bitop3:0x36
	v_lshlrev_b32_e32 v217, 4, v24
	v_add_u32_e32 v24, v22, v217
	ds_read_b128 v[24:27], v24 offset:49152
	s_waitcnt lgkmcnt(0)
	v_mfma_f32_32x32x16_bf16 v[64:79], v[24:27], v[116:119], v[64:79]
	v_add_u32_e32 v24, v28, v217
	ds_read_b128 v[24:27], v24
	s_waitcnt lgkmcnt(0)
	v_mfma_f32_32x32x16_bf16 v[48:63], v[24:27], v[116:119], v[48:63]
	v_bitop3_b32 v24, v23, v201, 5 bitop3:0x36
	v_lshlrev_b32_e32 v216, 4, v24
	v_add_u32_e32 v24, v22, v216
	ds_read_b128 v[24:27], v24 offset:49152
	s_waitcnt lgkmcnt(0)
	v_mfma_f32_32x32x16_bf16 v[64:79], v[24:27], v[122:125], v[64:79]
	v_add_u32_e32 v24, v28, v216
	ds_read_b128 v[24:27], v24
	s_waitcnt lgkmcnt(0)
	v_mfma_f32_32x32x16_bf16 v[48:63], v[24:27], v[122:125], v[48:63]
	v_bitop3_b32 v24, v23, v201, 6 bitop3:0x36
	v_lshlrev_b32_e32 v215, 4, v24
	v_add_u32_e32 v24, v22, v215
	ds_read_b128 v[24:27], v24 offset:49152
	s_waitcnt lgkmcnt(0)
	v_mfma_f32_32x32x16_bf16 v[64:79], v[24:27], v[164:167], v[64:79]
	v_add_u32_e32 v24, v28, v215
	ds_read_b128 v[24:27], v24
	s_waitcnt lgkmcnt(0)
	v_mfma_f32_32x32x16_bf16 v[48:63], v[24:27], v[164:167], v[48:63]
	v_bitop3_b32 v24, v23, v201, 7 bitop3:0x36
	v_lshlrev_b32_e32 v214, 4, v24
	v_add_u32_e32 v24, v22, v214
	ds_read_b128 v[24:27], v24 offset:49152
	s_waitcnt lgkmcnt(0)
	v_mfma_f32_32x32x16_bf16 v[64:79], v[24:27], v[160:163], v[64:79]
	v_add_u32_e32 v24, v28, v214
	ds_read_b128 v[24:27], v24
	s_waitcnt lgkmcnt(0)
	v_mfma_f32_32x32x16_bf16 v[48:63], v[24:27], v[160:163], v[48:63]
	v_bitop3_b32 v24, v23, v201, 8 bitop3:0x36
	v_lshlrev_b32_e32 v210, 4, v24
	v_add_u32_e32 v24, v22, v210
	ds_read_b128 v[24:27], v24 offset:49152
	s_waitcnt lgkmcnt(0)
	v_mfma_f32_32x32x16_bf16 v[64:79], v[24:27], v[156:159], v[64:79]
	v_add_u32_e32 v24, v28, v210
	ds_read_b128 v[24:27], v24
	s_waitcnt lgkmcnt(0)
	v_mfma_f32_32x32x16_bf16 v[48:63], v[24:27], v[156:159], v[48:63]
	v_bitop3_b32 v24, v23, v201, 9 bitop3:0x36
	v_lshlrev_b32_e32 v211, 4, v24
	v_add_u32_e32 v24, v22, v211
	ds_read_b128 v[24:27], v24 offset:49152
	s_waitcnt lgkmcnt(0)
	v_mfma_f32_32x32x16_bf16 v[64:79], v[24:27], v[152:155], v[64:79]
	v_add_u32_e32 v24, v28, v211
	ds_read_b128 v[24:27], v24
	s_waitcnt lgkmcnt(0)
	v_mfma_f32_32x32x16_bf16 v[48:63], v[24:27], v[152:155], v[48:63]
	v_bitop3_b32 v24, v23, v201, 10 bitop3:0x36
	v_lshlrev_b32_e32 v212, 4, v24
	v_add_u32_e32 v24, v22, v212
	ds_read_b128 v[24:27], v24 offset:49152
	s_waitcnt lgkmcnt(0)
	v_mfma_f32_32x32x16_bf16 v[64:79], v[24:27], v[148:151], v[64:79]
	v_add_u32_e32 v24, v28, v212
	ds_read_b128 v[24:27], v24
	s_waitcnt lgkmcnt(0)
	v_mfma_f32_32x32x16_bf16 v[48:63], v[24:27], v[148:151], v[48:63]
	v_bitop3_b32 v24, v23, v201, 11 bitop3:0x36
	v_lshlrev_b32_e32 v213, 4, v24
	v_add_u32_e32 v24, v22, v213
	ds_read_b128 v[24:27], v24 offset:49152
	s_waitcnt lgkmcnt(0)
	v_mfma_f32_32x32x16_bf16 v[64:79], v[24:27], v[128:131], v[64:79]
	v_add_u32_e32 v24, v28, v213
	ds_read_b128 v[24:27], v24
	s_waitcnt lgkmcnt(0)
	v_mfma_f32_32x32x16_bf16 v[48:63], v[24:27], v[128:131], v[48:63]
	v_bitop3_b32 v24, v23, v201, 12 bitop3:0x36
	v_lshlrev_b32_e32 v206, 4, v24
	v_add_u32_e32 v24, v22, v206
	ds_read_b128 v[24:27], v24 offset:49152
	s_waitcnt lgkmcnt(0)
	v_mfma_f32_32x32x16_bf16 v[64:79], v[24:27], v[144:147], v[64:79]
	v_add_u32_e32 v24, v28, v206
	ds_read_b128 v[24:27], v24
	s_waitcnt lgkmcnt(0)
	v_mfma_f32_32x32x16_bf16 v[48:63], v[24:27], v[144:147], v[48:63]
	v_bitop3_b32 v24, v23, v201, 13 bitop3:0x36
	v_lshlrev_b32_e32 v207, 4, v24
	v_add_u32_e32 v24, v22, v207
	ds_read_b128 v[24:27], v24 offset:49152
	s_waitcnt lgkmcnt(0)
	v_mfma_f32_32x32x16_bf16 v[64:79], v[24:27], v[140:143], v[64:79]
	v_add_u32_e32 v24, v28, v207
	ds_read_b128 v[24:27], v24
	s_waitcnt lgkmcnt(0)
	v_mfma_f32_32x32x16_bf16 v[48:63], v[24:27], v[140:143], v[48:63]
	v_bitop3_b32 v24, v23, v201, 14 bitop3:0x36
	v_lshlrev_b32_e32 v208, 4, v24
	v_add_u32_e32 v24, v22, v208
	ds_read_b128 v[24:27], v24 offset:49152
	v_bitop3_b32 v23, v23, v203, 15 bitop3:0x72
	v_lshlrev_b32_e32 v209, 4, v23
	v_add_u32_e32 v23, v22, v209
	s_waitcnt lgkmcnt(0)
	v_mfma_f32_32x32x16_bf16 v[64:79], v[24:27], v[132:135], v[64:79]
	v_add_u32_e32 v24, v28, v208
	ds_read_b128 v[24:27], v24
	s_waitcnt lgkmcnt(0)
	v_mfma_f32_32x32x16_bf16 v[48:63], v[24:27], v[132:135], v[48:63]
	ds_read_b128 v[24:27], v23 offset:49152
	v_add_u32_e32 v23, v28, v209
	v_add_u32_e32 v28, 0x18000, v22
	v_add_u32_e32 v29, v28, v213
	s_waitcnt lgkmcnt(0)
	v_mfma_f32_32x32x16_bf16 v[64:79], v[24:27], v[136:139], v[64:79]
	ds_read_b128 v[24:27], v23
	v_add_u32_e32 v23, s33, v20
	v_add_u32_e32 v20, v221, v21
	s_waitcnt lgkmcnt(0)
	v_mfma_f32_32x32x16_bf16 v[48:63], v[24:27], v[136:139], v[48:63]
	v_add_u32_e32 v24, v23, v21
	ds_read_b128 v[24:27], v24
	s_waitcnt lgkmcnt(0)
	v_mfma_f32_32x32x16_bf16 v[96:111], v[24:27], v[16:19], 0
	v_add_u32_e32 v24, v28, v21
	ds_read_b128 v[24:27], v24
	s_waitcnt lgkmcnt(0)
	v_mfma_f32_32x32x16_bf16 v[80:95], v[24:27], v[16:19], 0
	v_add_u32_e32 v24, v23, v202
	ds_read_b128 v[24:27], v24
	s_waitcnt lgkmcnt(0)
	v_mfma_f32_32x32x16_bf16 v[96:111], v[24:27], v[172:175], v[96:111]
	v_add_u32_e32 v24, v28, v202
	ds_read_b128 v[24:27], v24
	v_add_u32_e32 v202, v218, v202
	s_waitcnt lgkmcnt(0)
	v_mfma_f32_32x32x16_bf16 v[80:95], v[24:27], v[172:175], v[80:95]
	v_add_u32_e32 v24, v23, v220
	ds_read_b128 v[24:27], v24
	s_waitcnt lgkmcnt(0)
	v_mfma_f32_32x32x16_bf16 v[96:111], v[24:27], v[168:171], v[96:111]
	v_add_u32_e32 v24, v28, v220
	ds_read_b128 v[24:27], v24
	s_waitcnt lgkmcnt(0)
	v_mfma_f32_32x32x16_bf16 v[80:95], v[24:27], v[168:171], v[80:95]
	v_add_u32_e32 v24, v23, v219
	ds_read_b128 v[24:27], v24
	s_waitcnt lgkmcnt(0)
	v_mfma_f32_32x32x16_bf16 v[96:111], v[24:27], v[112:115], v[96:111]
	v_add_u32_e32 v24, v28, v219
	ds_read_b128 v[24:27], v24
	s_waitcnt lgkmcnt(0)
	v_mfma_f32_32x32x16_bf16 v[80:95], v[24:27], v[112:115], v[80:95]
	v_add_u32_e32 v24, v23, v217
	ds_read_b128 v[24:27], v24
	s_waitcnt lgkmcnt(0)
	v_mfma_f32_32x32x16_bf16 v[96:111], v[24:27], v[116:119], v[96:111]
	v_add_u32_e32 v24, v28, v217
	ds_read_b128 v[24:27], v24
	s_waitcnt lgkmcnt(0)
	v_mfma_f32_32x32x16_bf16 v[80:95], v[24:27], v[116:119], v[80:95]
	v_add_u32_e32 v24, v23, v216
	ds_read_b128 v[24:27], v24
	s_waitcnt lgkmcnt(0)
	v_mfma_f32_32x32x16_bf16 v[96:111], v[24:27], v[122:125], v[96:111]
	v_add_u32_e32 v24, v28, v216
	ds_read_b128 v[24:27], v24
	s_waitcnt lgkmcnt(0)
	v_mfma_f32_32x32x16_bf16 v[80:95], v[24:27], v[122:125], v[80:95]
	v_add_u32_e32 v24, v23, v215
	ds_read_b128 v[24:27], v24
	s_waitcnt lgkmcnt(0)
	v_mfma_f32_32x32x16_bf16 v[96:111], v[24:27], v[164:167], v[96:111]
	v_add_u32_e32 v24, v28, v215
	ds_read_b128 v[24:27], v24
	s_waitcnt lgkmcnt(0)
	v_mfma_f32_32x32x16_bf16 v[80:95], v[24:27], v[164:167], v[80:95]
	v_add_u32_e32 v24, v23, v214
	ds_read_b128 v[24:27], v24
	s_waitcnt lgkmcnt(0)
	v_mfma_f32_32x32x16_bf16 v[96:111], v[24:27], v[160:163], v[96:111]
	v_add_u32_e32 v24, v28, v214
	ds_read_b128 v[24:27], v24
	s_waitcnt lgkmcnt(0)
	v_mfma_f32_32x32x16_bf16 v[80:95], v[24:27], v[160:163], v[80:95]
	v_add_u32_e32 v24, v23, v210
	ds_read_b128 v[24:27], v24
	s_waitcnt lgkmcnt(0)
	v_mfma_f32_32x32x16_bf16 v[96:111], v[24:27], v[156:159], v[96:111]
	v_add_u32_e32 v24, v28, v210
	ds_read_b128 v[24:27], v24
	s_waitcnt lgkmcnt(0)
	v_mfma_f32_32x32x16_bf16 v[80:95], v[24:27], v[156:159], v[80:95]
	v_add_u32_e32 v24, v23, v211
	ds_read_b128 v[24:27], v24
	s_waitcnt lgkmcnt(0)
	v_mfma_f32_32x32x16_bf16 v[96:111], v[24:27], v[152:155], v[96:111]
	v_add_u32_e32 v24, v28, v211
	ds_read_b128 v[24:27], v24
	s_waitcnt lgkmcnt(0)
	v_mfma_f32_32x32x16_bf16 v[80:95], v[24:27], v[152:155], v[80:95]
	v_add_u32_e32 v24, v23, v212
	ds_read_b128 v[24:27], v24
	s_waitcnt lgkmcnt(0)
	v_mfma_f32_32x32x16_bf16 v[96:111], v[24:27], v[148:151], v[96:111]
	v_add_u32_e32 v24, v28, v212
	ds_read_b128 v[24:27], v24
	s_waitcnt lgkmcnt(0)
	v_mfma_f32_32x32x16_bf16 v[80:95], v[24:27], v[148:151], v[80:95]
	v_add_u32_e32 v24, v23, v213
	ds_read_b128 v[24:27], v24
	s_waitcnt lgkmcnt(0)
	v_mfma_f32_32x32x16_bf16 v[96:111], v[24:27], v[128:131], v[96:111]
	ds_read_b128 v[24:27], v29
	v_add_u32_e32 v29, v23, v206
	s_waitcnt lgkmcnt(0)
	v_mfma_f32_32x32x16_bf16 v[80:95], v[24:27], v[128:131], v[80:95]
	ds_read_b128 v[24:27], v29
	v_add_u32_e32 v29, v28, v206
	s_waitcnt lgkmcnt(0)
	v_mfma_f32_32x32x16_bf16 v[96:111], v[24:27], v[144:147], v[96:111]
	ds_read_b128 v[24:27], v29
	v_add_u32_e32 v29, v23, v207
	s_waitcnt lgkmcnt(0)
	v_mfma_f32_32x32x16_bf16 v[80:95], v[24:27], v[144:147], v[80:95]
	ds_read_b128 v[24:27], v29
	v_add_u32_e32 v29, v28, v207
	s_waitcnt lgkmcnt(0)
	v_mfma_f32_32x32x16_bf16 v[96:111], v[24:27], v[140:143], v[96:111]
	ds_read_b128 v[24:27], v29
	v_add_u32_e32 v29, v23, v208
	v_add_u32_e32 v23, v23, v209
	s_waitcnt lgkmcnt(0)
	v_mfma_f32_32x32x16_bf16 v[80:95], v[24:27], v[140:143], v[80:95]
	ds_read_b128 v[24:27], v29
	v_add_u32_e32 v29, v28, v208
	s_waitcnt lgkmcnt(0)
	v_mfma_f32_32x32x16_bf16 v[96:111], v[24:27], v[132:135], v[96:111]
	ds_read_b128 v[24:27], v29
	s_waitcnt lgkmcnt(0)
	v_mfma_f32_32x32x16_bf16 v[80:95], v[24:27], v[132:135], v[80:95]
	ds_read_b128 v[24:27], v23
	v_add_u32_e32 v23, v28, v209
	s_waitcnt lgkmcnt(0)
	v_mfma_f32_32x32x16_bf16 v[96:111], v[24:27], v[136:139], v[96:111]
	ds_read_b128 v[24:27], v23
	s_waitcnt lgkmcnt(0)
	v_mfma_f32_32x32x16_bf16 v[80:95], v[24:27], v[136:139], v[80:95]
	ds_read_b128 v[24:27], v20
	v_add_u32_e32 v20, v218, v21
	ds_read_b128 v[20:23], v20
	s_waitcnt lgkmcnt(1)
	v_mfma_f32_32x32x16_bf16 v[32:47], v[24:27], v[16:19], 0
	v_mfma_f32_32x32x16_bf16 v[32:47], v[222:225], v[172:175], v[32:47]
	ds_read_b128 v[222:225], v202
	v_add_u32_e32 v202, v221, v220
	ds_read_b128 v[226:229], v202
	s_waitcnt lgkmcnt(2)
	v_mfma_f32_32x32x16_bf16 v[16:31], v[20:23], v[16:19], 0
	s_waitcnt lgkmcnt(1)
	v_mfma_f32_32x32x16_bf16 v[16:31], v[222:225], v[172:175], v[16:31]
	v_lshl_add_u64 v[174:175], v[126:127], 0, v[180:181]
	v_add_u32_e32 v126, v218, v220
	ds_read_b128 v[222:225], v126
	v_mov_b32_e32 v126, v177
	v_add_u32_e32 v177, v221, v219
	v_mov_b32_e32 v127, v178
	v_lshl_add_u64 v[172:173], v[188:189], 0, v[184:185]
	s_waitcnt lgkmcnt(1)
	v_mfma_f32_32x32x16_bf16 v[32:47], v[226:229], v[168:171], v[32:47]
	ds_read_b128 v[226:229], v177
	v_mov_b32_e32 v177, v179
	v_add_f32_e64 v126, v126, v176
	v_add_f32_e64 v127, v127, v177
	v_lshl_add_u64 v[188:189], v[120:121], 0, v[186:187]
	v_add_f32_e32 v126, v126, v127
	v_add_u32_e32 v127, v218, v219
	ds_read_b128 v[176:179], v127
	s_waitcnt lgkmcnt(2)
	v_mfma_f32_32x32x16_bf16 v[16:31], v[222:225], v[168:171], v[16:31]
	v_fmamk_f32 v126, v126, 0x3b800000, v198
	v_rsq_f32_e32 v126, v126
	v_lshlrev_b32_e32 v120, 8, v200
	v_mov_b32_e32 v121, v181
	v_lshl_add_u64 v[170:171], s[4:5], 0, v[120:121]
	v_mul_f32_e32 v168, 0x3dd53b94, v126
	v_lshlrev_b32_e32 v169, 3, v204
	v_add_u32_e32 v120, v221, v217
	ds_read_b128 v[222:225], v120
	v_pk_mul_f32 v[64:65], v[168:169], v[64:65] op_sel_hi:[0,1]
	s_waitcnt lgkmcnt(2)
	v_mfma_f32_32x32x16_bf16 v[32:47], v[226:229], v[112:115], v[32:47]
	v_mul_f32_e64 v66, v168, v66
	v_mul_f32_e64 v67, v168, v67
	v_mul_f32_e64 v68, v168, v68
	v_mul_f32_e64 v69, v168, v69
	v_mul_f32_e64 v70, v168, v70
	v_mul_f32_e64 v71, v168, v71
	v_pk_mul_f32 v[48:49], v[168:169], v[48:49] op_sel_hi:[0,1]
	v_cvt_pk_bf16_f32 v120, v48, v49
	v_add_u32_e32 v48, v221, v215
	v_pk_mul_f32 v[78:79], v[168:169], v[78:79] op_sel_hi:[0,1]
	s_waitcnt lgkmcnt(1)
	v_mfma_f32_32x32x16_bf16 v[16:31], v[176:179], v[112:115], v[16:31]
	v_cvt_pk_bf16_f32 v112, v64, v65
	v_add_u32_e32 v64, v218, v217
	v_cvt_pk_bf16_f32 v113, v66, v67
	ds_read_b128 v[64:67], v64
	v_cvt_pk_bf16_f32 v114, v68, v69
	v_add_u32_e32 v68, v221, v216
	v_cvt_pk_bf16_f32 v115, v70, v71
	ds_read_b128 v[68:71], v68
	s_waitcnt lgkmcnt(2)
	v_mfma_f32_32x32x16_bf16 v[32:47], v[222:225], v[116:119], v[32:47]
	v_mul_f32_e64 v52, v168, v52
	v_mul_f32_e64 v53, v168, v53
	v_mul_f32_e64 v54, v168, v54
	v_mul_f32_e64 v55, v168, v55
	v_mul_f32_e64 v72, v168, v72
	v_mul_f32_e64 v73, v168, v73
	v_pk_mul_f32 v[60:61], v[168:169], v[60:61] op_sel_hi:[0,1]
	v_pk_mul_f32 v[62:63], v[168:169], v[62:63] op_sel_hi:[0,1]
	v_cvt_pk_bf16_f32 v126, v60, v61
	v_cvt_pk_bf16_f32 v127, v62, v63
	s_waitcnt lgkmcnt(1)
	v_mfma_f32_32x32x16_bf16 v[16:31], v[64:67], v[116:119], v[16:31]
	v_mul_f32_e64 v64, v168, v74
	v_mul_f32_e64 v65, v168, v75
	v_cvt_pk_bf16_f32 v117, v64, v65
	v_add_u32_e32 v64, v218, v216
	ds_read_b128 v[64:67], v64
	v_cvt_pk_bf16_f32 v119, v78, v79
	v_pk_mul_f32 v[78:79], v[168:169], v[88:89] op_sel_hi:[0,1]
	v_cvt_pk_bf16_f32 v116, v72, v73
	s_waitcnt lgkmcnt(1)
	v_mfma_f32_32x32x16_bf16 v[32:47], v[68:71], v[122:125], v[32:47]
	v_mul_f32_e64 v68, v168, v50
	v_mul_f32_e64 v69, v168, v51
	ds_read_b128 v[48:51], v48
	v_mul_f32_e64 v70, v168, v86
	v_mul_f32_e64 v71, v168, v87
	v_add_u32_e32 v86, v218, v213
	ds_read_b128 v[86:89], v86
	v_pk_mul_f32 v[60:61], v[168:169], v[100:101] op_sel_hi:[0,1]
	v_pk_mul_f32 v[62:63], v[168:169], v[102:103] op_sel_hi:[0,1]
	s_waitcnt lgkmcnt(2)
	v_mfma_f32_32x32x16_bf16 v[16:31], v[64:67], v[122:125], v[16:31]
	v_cvt_pk_bf16_f32 v122, v52, v53
	v_add_u32_e32 v52, v218, v215
	v_cvt_pk_bf16_f32 v123, v54, v55
	ds_read_b128 v[52:55], v52
	v_mul_f32_e64 v64, v168, v98
	v_mul_f32_e64 v65, v168, v99
	v_cvt_pk_bf16_f32 v98, v60, v61
	v_cvt_pk_bf16_f32 v99, v62, v63
	s_waitcnt lgkmcnt(2)
	v_mfma_f32_32x32x16_bf16 v[32:47], v[48:51], v[164:167], v[32:47]
	v_mul_f32_e64 v48, v168, v56
	v_mul_f32_e64 v49, v168, v57
	v_mul_f32_e64 v50, v168, v58
	v_mul_f32_e64 v51, v168, v59
	v_cvt_pk_bf16_f32 v124, v48, v49
	v_add_u32_e32 v48, v221, v214
	v_cvt_pk_bf16_f32 v125, v50, v51
	ds_read_b128 v[48:51], v48
	v_and_b32_e32 v58, 32, v205
	s_waitcnt lgkmcnt(1)
	v_mfma_f32_32x32x16_bf16 v[16:31], v[52:55], v[164:167], v[16:31]
	v_add_u32_e32 v52, v218, v214
	ds_read_b128 v[52:55], v52
	v_mov_b32_e32 v59, v181
	v_lshl_add_u64 v[72:73], v[170:171], 0, v[58:59]
	v_mul_f32_e64 v56, v168, v96
	v_mul_f32_e64 v57, v168, v97
	v_cvt_pk_bf16_f32 v96, v56, v57
	v_add_u32_e32 v56, v221, v210
	s_waitcnt lgkmcnt(1)
	v_mfma_f32_32x32x16_bf16 v[32:47], v[48:51], v[160:163], v[32:47]
	global_load_dwordx4 v[48:51], v[72:73], off offset:16
	ds_read_b128 v[56:59], v56
	v_cvt_pk_bf16_f32 v97, v64, v65
	v_mul_f32_e64 v64, v168, v106
	v_mul_f32_e64 v65, v168, v107
	v_cvt_pk_bf16_f32 v101, v64, v65
	v_cvt_pk_bf16_f32 v121, v68, v69
	v_pk_mul_f32 v[68:69], v[168:169], v[108:109] op_sel_hi:[0,1]
	s_waitcnt lgkmcnt(1)
	v_mfma_f32_32x32x16_bf16 v[16:31], v[52:55], v[160:163], v[16:31]
	v_add_u32_e32 v52, v221, v211
	ds_read_b128 v[60:63], v52
	global_load_dwordx4 v[52:55], v[72:73], off
	v_cvt_pk_bf16_f32 v102, v68, v69
	v_mul_f32_e64 v68, v168, v84
	v_mul_f32_e64 v69, v168, v85
	v_cvt_pk_bf16_f32 v106, v68, v69
	v_add_u32_e32 v68, v221, v207
	s_waitcnt lgkmcnt(1)
	v_mfma_f32_32x32x16_bf16 v[32:47], v[56:59], v[156:159], v[32:47]
	v_mul_f32_e64 v58, v168, v104
	v_mul_f32_e64 v59, v168, v105
	v_cvt_pk_bf16_f32 v100, v58, v59
	v_add_u32_e32 v58, v221, v212
	ds_read_b128 v[64:67], v58
	v_pk_mul_f32 v[56:57], v[168:169], v[110:111] op_sel_hi:[0,1]
	v_cvt_pk_bf16_f32 v103, v56, v57
	v_add_u32_e32 v56, v221, v213
	s_waitcnt lgkmcnt(1)
	v_mfma_f32_32x32x16_bf16 v[32:47], v[60:63], v[152:155], v[32:47]
	ds_read_b128 v[60:63], v56
	v_cvt_pk_bf16_f32 v107, v70, v71
	ds_read_b128 v[68:71], v68
	v_mul_f32_e64 v76, v168, v76
	v_mul_f32_e64 v77, v168, v77
	v_cvt_pk_bf16_f32 v118, v76, v77
	v_pk_mul_f32 v[74:75], v[168:169], v[92:93] op_sel_hi:[0,1]
	v_pk_mul_f32 v[76:77], v[168:169], v[94:95] op_sel_hi:[0,1]
	s_waitcnt lgkmcnt(2)
	v_mfma_f32_32x32x16_bf16 v[32:47], v[64:67], v[148:151], v[32:47]
	v_mul_f32_e64 v64, v168, v80
	v_mul_f32_e64 v65, v168, v81
	v_mul_f32_e64 v66, v168, v82
	v_mul_f32_e64 v67, v168, v83
	v_cvt_pk_bf16_f32 v104, v64, v65
	v_add_u32_e32 v64, v221, v206
	v_cvt_pk_bf16_f32 v105, v66, v67
	ds_read_b128 v[64:67], v64
	global_load_dwordx4 v[56:59], v[72:73], off offset:80
	s_waitcnt lgkmcnt(2)
	v_mfma_f32_32x32x16_bf16 v[32:47], v[60:63], v[128:131], v[32:47]
	v_cvt_pk_bf16_f32 v110, v74, v75
	v_cvt_pk_bf16_f32 v111, v76, v77
	v_cvt_pk_bf16_f32 v108, v78, v79
	global_load_dwordx4 v[60:63], v[72:73], off offset:64
	global_load_dwordx4 v[164:167], v[72:73], off offset:128
	v_add_u32_e32 v94, v218, v207
	s_movk_i32 s4, 0x180
	s_waitcnt lgkmcnt(0)
	v_mfma_f32_32x32x16_bf16 v[32:47], v[64:67], v[144:147], v[32:47]
	v_mul_f32_e64 v64, v168, v90
	v_mul_f32_e64 v65, v168, v91
	v_cvt_pk_bf16_f32 v109, v64, v65
	v_add_u32_e32 v64, v221, v208
	ds_read_b128 v[64:67], v64
	v_add_u32_e32 v90, v218, v206
	ds_read_b128 v[90:93], v90
	v_or_b32_e32 v202, s6, v203
	v_mfma_f32_32x32x16_bf16 v[32:47], v[68:71], v[140:143], v[32:47]
	v_add_u32_e32 v68, v218, v210
	ds_read_b128 v[74:77], v68
	v_add_u32_e32 v68, v218, v211
	v_add_u32_e32 v69, v221, v209
	ds_read_b128 v[78:81], v68
	ds_read_b128 v[82:85], v69
	v_add_u32_e32 v68, v218, v212
	s_waitcnt lgkmcnt(4)
	v_mfma_f32_32x32x16_bf16 v[32:47], v[64:67], v[132:135], v[32:47]
	global_load_dwordx4 v[64:67], v[72:73], off offset:144
	ds_read_b128 v[68:71], v68
	s_sub_i32 s5, 0, s25
	s_waitcnt lgkmcnt(1)
	v_mfma_f32_32x32x16_bf16 v[32:47], v[82:85], v[136:139], v[32:47]
	ds_read_b128 v[82:85], v94
	v_add_u32_e32 v94, v218, v208
	ds_read_b128 v[160:163], v94
	v_add_u32_e32 v94, v218, v209
	ds_read_b128 v[176:179], v94
	s_nop 6
	v_mul_f32_e32 v36, v168, v36
	v_mfma_f32_32x32x16_bf16 v[16:31], v[74:77], v[156:159], v[16:31]
	v_mul_f32_e32 v74, v168, v37
	s_waitcnt vmcnt(5)
	v_pk_mul_f32 v[74:75], v[74:75], v[48:49] op_sel:[0,1] op_sel_hi:[0,0]
	v_pk_fma_f32 v[76:77], v[36:37], v[48:49], v[74:75] neg_lo:[0,0,1] neg_hi:[0,0,1]
	v_pk_fma_f32 v[48:49], v[36:37], v[48:49], v[74:75] op_sel_hi:[0,1,1]
	v_mul_f32_e32 v36, v168, v39
	v_mul_f32_e32 v48, v168, v38
	v_pk_mul_f32 v[74:75], v[36:37], v[50:51] op_sel:[0,1] op_sel_hi:[0,0]
	global_load_dwordx4 v[36:39], v[72:73], off offset:208
	v_mfma_f32_32x32x16_bf16 v[16:31], v[78:81], v[152:155], v[16:31]
	v_fma_f32 v78, v48, v50, -v74
	v_fma_f32 v79, v49, v51, -v75
	v_fma_f32 v50, v48, v50, v74
	v_fma_f32 v51, v48, v51, v75
	v_mul_f32_e32 v48, v168, v33
	v_mul_f32_e32 v32, v168, v32
	s_waitcnt vmcnt(5)
	v_pk_mul_f32 v[74:75], v[48:49], v[52:53] op_sel:[0,1] op_sel_hi:[0,0]
	v_pk_fma_f32 v[80:81], v[32:33], v[52:53], v[74:75] neg_lo:[0,0,1] neg_hi:[0,0,1]
	v_pk_fma_f32 v[52:53], v[32:33], v[52:53], v[74:75] op_sel_hi:[0,1,1]
	v_mul_f32_e32 v48, v168, v34
	v_mul_f32_e32 v50, v168, v35
	global_load_dwordx4 v[32:35], v[72:73], off offset:192
	s_waitcnt lgkmcnt(3)
	v_mfma_f32_32x32x16_bf16 v[16:31], v[68:71], v[148:151], v[16:31]
	v_mul_f32_e64 v68, v50, v55
	v_mul_f32_e64 v69, v50, v54
	v_fma_f32 v70, v48, v54, -v68
	v_fma_f32 v71, v49, v55, -v69
	v_fma_f32 v54, v48, v54, v68
	v_fma_f32 v55, v48, v55, v69
	v_mul_f32_e32 v48, v168, v45
	v_mul_f32_e32 v44, v168, v44
	v_mul_f32_e32 v40, v168, v40
	v_mov_b32_e32 v158, 0
	v_mfma_f32_32x32x16_bf16 v[16:31], v[86:89], v[128:131], v[16:31]
	v_cvt_pk_bf16_f32 v130, v76, v49
	v_cvt_pk_bf16_f32 v131, v78, v51
	v_cvt_pk_bf16_f32 v128, v80, v53
	v_cvt_pk_bf16_f32 v129, v70, v55
	v_mov_b32_e32 v157, 0
	s_mov_b32 s101, 1
	s_waitcnt lgkmcnt(0)
	s_barrier
	v_mfma_f32_32x32x16_bf16 v[16:31], v[90:93], v[144:147], v[16:31]
	v_lshlrev_b32_e32 v145, 2, v204
	s_waitcnt vmcnt(5)
	v_pk_mul_f32 v[48:49], v[48:49], v[56:57] op_sel:[0,1] op_sel_hi:[0,0]
	v_pk_fma_f32 v[50:51], v[44:45], v[56:57], v[48:49] neg_lo:[0,0,1] neg_hi:[0,0,1]
	v_pk_fma_f32 v[44:45], v[44:45], v[56:57], v[48:49] op_sel_hi:[0,1,1]
	v_mul_f32_e32 v44, v168, v46
	v_mul_f32_e32 v46, v168, v47
	v_pk_mul_f32 v[46:47], v[46:47], v[58:59] op_sel:[0,1] op_sel_hi:[0,0]
	v_mfma_f32_32x32x16_bf16 v[16:31], v[82:85], v[140:143], v[16:31]
	v_fma_f32 v48, v44, v58, -v46
	v_fma_f32 v49, v45, v59, -v47
	v_fma_f32 v46, v44, v58, v46
	v_fma_f32 v47, v44, v59, v47
	v_mul_f32_e32 v44, v168, v41
	s_waitcnt vmcnt(4)
	v_pk_mul_f32 v[52:53], v[44:45], v[60:61] op_sel:[0,1] op_sel_hi:[0,0]
	v_pk_fma_f32 v[54:55], v[40:41], v[60:61], v[52:53] neg_lo:[0,0,1] neg_hi:[0,0,1]
	v_pk_fma_f32 v[40:41], v[40:41], v[60:61], v[52:53] op_sel_hi:[0,1,1]
	v_mul_f32_e32 v40, v168, v42
	v_mfma_f32_32x32x16_bf16 v[16:31], v[160:163], v[132:135], v[16:31]
	v_mul_f32_e32 v42, v168, v43
	v_pk_mul_f32 v[42:43], v[42:43], v[62:63] op_sel:[0,1] op_sel_hi:[0,0]
	v_pk_fma_f32 v[52:53], v[40:41], v[62:63], v[42:43] neg_lo:[0,0,1] neg_hi:[0,0,1]
	v_pk_fma_f32 v[42:43], v[40:41], v[62:63], v[42:43] op_sel_hi:[0,1,1]
	v_cvt_pk_bf16_f32 v132, v54, v41
	v_cvt_pk_bf16_f32 v133, v52, v43
	v_cvt_pk_bf16_f32 v134, v50, v45
	v_mfma_f32_32x32x16_bf16 v[16:31], v[176:179], v[136:139], v[16:31]
	v_cvt_pk_bf16_f32 v135, v48, v47
	v_mov_b64_e32 v[62:63], v[14:15]
	v_mov_b64_e32 v[60:61], v[12:13]
	v_mov_b64_e32 v[58:59], v[10:11]
	v_mov_b64_e32 v[56:57], v[8:9]
	v_mov_b64_e32 v[54:55], v[6:7]
	v_mov_b64_e32 v[52:53], v[4:5]
	s_nop 4
	v_mul_f32_e32 v40, v168, v21
	v_mul_f32_e32 v20, v168, v20
	s_waitcnt vmcnt(2)
	v_pk_mul_f32 v[40:41], v[40:41], v[64:65] op_sel:[0,1] op_sel_hi:[0,0]
	v_pk_fma_f32 v[42:43], v[20:21], v[64:65], v[40:41] neg_lo:[0,0,1] neg_hi:[0,0,1]
	v_pk_fma_f32 v[20:21], v[20:21], v[64:65], v[40:41] op_sel_hi:[0,1,1]
	v_mul_f32_e32 v20, v168, v22
	v_mul_f32_e32 v22, v168, v23
	v_pk_mul_f32 v[22:23], v[22:23], v[66:67] op_sel:[0,1] op_sel_hi:[0,0]
	v_pk_fma_f32 v[40:41], v[20:21], v[66:67], v[22:23] neg_lo:[0,0,1] neg_hi:[0,0,1]
	v_pk_fma_f32 v[22:23], v[20:21], v[66:67], v[22:23] op_sel_hi:[0,1,1]
	v_mul_f32_e32 v20, v168, v17
	v_mul_f32_e32 v16, v168, v16
	v_pk_mul_f32 v[44:45], v[20:21], v[164:165] op_sel:[0,1] op_sel_hi:[0,0]
	v_pk_fma_f32 v[46:47], v[16:17], v[164:165], v[44:45] neg_lo:[0,0,1] neg_hi:[0,0,1]
	v_pk_fma_f32 v[16:17], v[16:17], v[164:165], v[44:45] op_sel_hi:[0,1,1]
	v_mul_f32_e32 v16, v168, v18
	v_mul_f32_e32 v18, v168, v19
	v_pk_mul_f32 v[18:19], v[18:19], v[166:167] op_sel:[0,1] op_sel_hi:[0,0]
	v_pk_fma_f32 v[44:45], v[16:17], v[166:167], v[18:19] neg_lo:[0,0,1] neg_hi:[0,0,1]
	v_pk_fma_f32 v[18:19], v[16:17], v[166:167], v[18:19] op_sel_hi:[0,1,1]
	v_mul_f32_e32 v18, v168, v29
	v_cvt_pk_bf16_f32 v137, v44, v19
	v_mul_f32_e32 v16, v168, v28
	s_waitcnt vmcnt(1)
	v_pk_mul_f32 v[18:19], v[18:19], v[36:37] op_sel:[0,1] op_sel_hi:[0,0]
	v_cvt_pk_bf16_f32 v136, v46, v17
	v_cvt_pk_bf16_f32 v138, v42, v21
	v_pk_fma_f32 v[20:21], v[16:17], v[36:37], v[18:19] neg_lo:[0,0,1] neg_hi:[0,0,1]
	v_pk_fma_f32 v[16:17], v[16:17], v[36:37], v[18:19] op_sel_hi:[0,1,1]
	v_mul_f32_e32 v18, v168, v31
	v_mul_f32_e32 v16, v168, v30
	v_pk_mul_f32 v[18:19], v[18:19], v[38:39] op_sel:[0,1] op_sel_hi:[0,0]
	v_cvt_pk_bf16_f32 v139, v40, v23
	v_pk_fma_f32 v[22:23], v[16:17], v[38:39], v[18:19] neg_lo:[0,0,1] neg_hi:[0,0,1]
	v_pk_fma_f32 v[18:19], v[16:17], v[38:39], v[18:19] op_sel_hi:[0,1,1]
	v_mul_f32_e32 v18, v168, v25
	v_mul_f32_e32 v16, v168, v24
	s_waitcnt vmcnt(0)
	v_pk_mul_f32 v[24:25], v[18:19], v[32:33] op_sel:[0,1] op_sel_hi:[0,0]
	v_mul_f32_e32 v18, v168, v27
	v_pk_fma_f32 v[28:29], v[16:17], v[32:33], v[24:25] neg_lo:[0,0,1] neg_hi:[0,0,1]
	v_pk_fma_f32 v[24:25], v[16:17], v[32:33], v[24:25] op_sel_hi:[0,1,1]
	v_mul_f32_e32 v16, v168, v26
	v_pk_mul_f32 v[26:27], v[18:19], v[34:35] op_sel:[0,1] op_sel_hi:[0,0]
	v_pk_fma_f32 v[30:31], v[16:17], v[34:35], v[26:27] neg_lo:[0,0,1] neg_hi:[0,0,1]
	v_pk_fma_f32 v[26:27], v[16:17], v[34:35], v[26:27] op_sel_hi:[0,1,1]
	v_cvt_pk_bf16_f32 v142, v20, v17
	v_lshrrev_b32_e32 v17, 1, v203
	v_mad_u32_u24 v16, v200, s4, 0
	v_bfe_u32 v18, v203, 1, 3
	v_bitop3_b32 v17, v204, v17, 7 bitop3:0x78
	v_lshl_add_u32 v147, v17, 4, v16
	v_bitop3_b32 v17, v204, v18, 2 bitop3:0x36
	v_lshl_add_u32 v148, v17, 4, v16
	v_bitop3_b32 v17, v204, v18, 4 bitop3:0x36
	v_lshl_add_u32 v149, v17, 4, v16
	v_bitop3_b32 v17, v204, v18, 6 bitop3:0x36
	v_lshl_add_u32 v150, v17, 4, v16
	v_lshrrev_b32_e32 v16, 3, v202
	v_bfe_u32 v17, v202, 3, 1
	v_and_b32_e32 v16, 2, v16
	v_bfe_u32 v18, v203, 1, 1
	v_bfe_u32 v20, v203, 2, 1
	v_lshlrev_b32_e32 v21, 3, v17
	v_cvt_pk_bf16_f32 v143, v22, v19
	v_or_b32_e32 v19, v16, v18
	v_or3_b32 v20, v21, v20, v145
	v_lshlrev_b32_e32 v21, 1, v204
	v_bitop3_b32 v16, v16, v21, v18 bitop3:0x36
	v_bitop3_b32 v18, v21, v19, 1 bitop3:0x36
	v_cvt_f32_ubyte0_e32 v21, s25
	v_lshlrev_b32_e32 v22, 3, v203
	v_lshlrev_b32_e32 v17, 6, v17
	v_lshlrev_b32_e32 v18, 4, v18
	v_rcp_iflag_f32_e32 v21, v21
	v_and_b32_e32 v22, 8, v22
	v_mad_u32_u24 v20, v20, s4, 0
	v_or_b32_e32 v19, v18, v17
	v_lshl_add_u32 v16, v16, 4, v20
	v_add3_u32 v152, v20, v19, v22
	v_xor_b32_e32 v19, 64, v17
	v_add3_u32 v151, v16, v17, v22
	v_add3_u32 v153, v16, v19, v22
	v_bitop3_b32 v16, v18, v17, 64 bitop3:0xf6
	v_add3_u32 v154, v20, v16, v22
	v_mul_f32_e32 v16, 0x4f7ffffe, v21
	v_cvt_u32_f32_e32 v16, v16
	s_abs_i32 s4, s89
	v_cvt_pk_bf16_f32 v140, v28, v25
	v_cvt_pk_bf16_f32 v141, v30, v27
	v_readfirstlane_b32 s6, v16
	s_mul_i32 s5, s5, s6
	s_mul_hi_u32 s5, s6, s5
	s_add_i32 s6, s6, s5
	s_mul_hi_u32 s5, s4, s6
	s_mul_i32 s6, s5, s25
	s_sub_i32 s4, s4, s6
	s_add_i32 s6, s5, 1
	s_sub_i32 s7, s4, s25
	s_cmp_ge_u32 s4, s25
	s_cselect_b32 s5, s6, s5
	s_cselect_b32 s4, s7, s4
	s_add_i32 s6, s5, 1
	s_cmp_ge_u32 s4, s25
	s_cselect_b32 s4, s6, s5
	s_xor_b32 s12, s4, s11
	s_sub_i32 s8, s12, s11
	s_mul_i32 s4, s8, s25
	s_sub_i32 s4, s89, s4
	s_lshl_b32 s6, s4, 5
	s_ashr_i32 s7, s6, 31
	s_lshl_b64 s[4:5], s[6:7], 2
	s_add_u32 s4, s68, s4
	s_addc_u32 s5, s69, s5
	v_lshl_or_b32 v16, s12, 6, v196
	s_lshl_b32 s7, s11, 6
	v_subrev_u32_e32 v155, s7, v16
	s_add_i32 s7, s29, s21
	v_add_u32_e32 v16, s7, v200
	v_sub_u32_e32 v156, v16, v145
	v_mov_b64_e32 v[46:47], v[14:15]
	v_mov_b64_e32 v[30:31], v[14:15]
	s_movk_i32 s7, 0x7f
	s_mov_b32 s11, 3
	s_mov_b32 s12, s40
	v_mov_b64_e32 v[44:45], v[12:13]
	v_mov_b64_e32 v[42:43], v[10:11]
	v_mov_b64_e32 v[40:41], v[8:9]
	v_mov_b64_e32 v[38:39], v[6:7]
	v_mov_b64_e32 v[36:37], v[4:5]
	v_mov_b64_e32 v[34:35], v[2:3]
	v_mov_b64_e32 v[32:33], v[0:1]
	v_mov_b64_e32 v[50:51], v[2:3]
	v_mov_b64_e32 v[48:49], v[0:1]
	v_mov_b64_e32 v[28:29], v[12:13]
	v_mov_b64_e32 v[26:27], v[10:11]
	v_mov_b64_e32 v[24:25], v[8:9]
	v_mov_b64_e32 v[22:23], v[6:7]
	v_mov_b64_e32 v[20:21], v[4:5]
	v_mov_b64_e32 v[18:19], v[2:3]
	v_mov_b64_e32 v[16:17], v[0:1]
	s_branch .LBB0_1238

.LBB0_1244:
	s_cmp_lg_u32 s101, 0
	s_cbranch_scc1 .Lf_a

.Lf_a:
	s_nop 7
	v_exp_f32_e32 v240, v80
	v_exp_f32_e32 v241, v81
	v_exp_f32_e32 v242, v82
	v_exp_f32_e32 v243, v83
	v_exp_f32_e32 v244, v84
	v_exp_f32_e32 v245, v85
	v_exp_f32_e32 v246, v86
	v_exp_f32_e32 v247, v87
	v_add_f32_e32 v159, v240, v241
	v_add_f32_e32 v159, v242, v159
	v_add_f32_e32 v159, v243, v159
	v_add_f32_e32 v159, v244, v159
	v_add_f32_e32 v159, v245, v159
	v_add_f32_e32 v159, v246, v159
	v_add_f32_e32 v159, v247, v159
	v_cvt_pk_bf16_f32 v224, v240, v241
	v_cvt_pk_bf16_f32 v225, v244, v245
	v_cvt_pk_bf16_f32 v226, v242, v243
	v_cvt_pk_bf16_f32 v227, v246, v247
	v_exp_f32_e32 v240, v88
	v_exp_f32_e32 v241, v89
	v_exp_f32_e32 v242, v90
	v_exp_f32_e32 v243, v91
	v_exp_f32_e32 v244, v92
	v_exp_f32_e32 v245, v93
	v_exp_f32_e32 v246, v94
	v_exp_f32_e32 v247, v95
	v_add_f32_e32 v159, v240, v159
	v_add_f32_e32 v159, v241, v159
	v_add_f32_e32 v159, v242, v159
	v_add_f32_e32 v159, v243, v159
	v_add_f32_e32 v159, v244, v159
	v_add_f32_e32 v159, v245, v159
	v_add_f32_e32 v159, v246, v159
	v_add_f32_e32 v159, v247, v159
	v_cvt_pk_bf16_f32 v228, v240, v241
	v_cvt_pk_bf16_f32 v229, v244, v245
	v_cvt_pk_bf16_f32 v230, v242, v243
	v_cvt_pk_bf16_f32 v231, v246, v247
	v_exp_f32_e32 v240, v64
	v_exp_f32_e32 v241, v65
	v_exp_f32_e32 v242, v66
	v_exp_f32_e32 v243, v67
	v_exp_f32_e32 v244, v68
	v_exp_f32_e32 v245, v69
	v_exp_f32_e32 v246, v70
	v_exp_f32_e32 v247, v71
	v_add_f32_e32 v159, v240, v159
	v_add_f32_e32 v159, v241, v159
	v_add_f32_e32 v159, v242, v159
	v_add_f32_e32 v159, v243, v159
	v_add_f32_e32 v159, v244, v159
	v_add_f32_e32 v159, v245, v159
	v_add_f32_e32 v159, v246, v159
	v_add_f32_e32 v159, v247, v159
	v_cvt_pk_bf16_f32 v232, v240, v241
	v_cvt_pk_bf16_f32 v233, v244, v245
	v_cvt_pk_bf16_f32 v234, v242, v243
	v_cvt_pk_bf16_f32 v235, v246, v247
	v_exp_f32_e32 v240, v72
	v_exp_f32_e32 v241, v73
	v_exp_f32_e32 v242, v74
	v_exp_f32_e32 v243, v75
	v_exp_f32_e32 v244, v76
	v_exp_f32_e32 v245, v77
	v_exp_f32_e32 v246, v78
	v_exp_f32_e32 v247, v79
	v_add_f32_e32 v159, v240, v159
	v_add_f32_e32 v159, v241, v159
	v_add_f32_e32 v159, v242, v159
	v_add_f32_e32 v159, v243, v159
	v_add_f32_e32 v159, v244, v159
	v_add_f32_e32 v159, v245, v159
	v_add_f32_e32 v159, v246, v159
	v_add_f32_e32 v159, v247, v159
	v_cvt_pk_bf16_f32 v236, v240, v241
	v_cvt_pk_bf16_f32 v237, v244, v245
	v_cvt_pk_bf16_f32 v238, v242, v243
	v_cvt_pk_bf16_f32 v239, v246, v247
	v_cmp_gt_f32_e32 vcc, 0x7149f2ca, v159
	s_cmp_eq_u64 vcc, exec
	s_cbranch_scc0 .Lf_a_fail
	v_add_f32_e32 v158, v158, v159
	v_add_u32_e32 v146, s14, v151
	v_add_u32_e32 v161, s14, v152
	ds_read_b64_tr_b16 v[80:81], v146
	ds_read_b64_tr_b16 v[82:83], v161 offset:768
	ds_read_b64_tr_b16 v[84:85], v146 offset:6144
	ds_read_b64_tr_b16 v[86:87], v161 offset:6912
	ds_read_b64_tr_b16 v[88:89], v146 offset:12288
	ds_read_b64_tr_b16 v[90:91], v161 offset:13056
	ds_read_b64_tr_b16 v[92:93], v146 offset:18432
	ds_read_b64_tr_b16 v[94:95], v161 offset:19200
	s_waitcnt lgkmcnt(6)
	v_mfma_f32_32x32x16_bf16 v[48:63], v[80:83], v[224:227], v[48:63]
	v_add_u32_e32 v166, s14, v153
	v_add_u32_e32 v167, s14, v154
	ds_read_b64_tr_b16 v[162:163], v166
	ds_read_b64_tr_b16 v[164:165], v167 offset:768
	ds_read_b64_tr_b16 v[176:177], v166 offset:6144
	ds_read_b64_tr_b16 v[178:179], v167 offset:6912
	ds_read_b64_tr_b16 v[204:205], v166 offset:12288
	ds_read_b64_tr_b16 v[206:207], v167 offset:13056
	ds_read_b64_tr_b16 v[208:209], v166 offset:18432
	ds_read_b64_tr_b16 v[210:211], v167 offset:19200
	s_waitcnt lgkmcnt(12)
	v_mfma_f32_32x32x16_bf16 v[48:63], v[84:87], v[228:231], v[48:63]
	s_add_i32 s14, s10, -2
	s_and_b32 s14, s14, 3
	s_mulk_i32 s14, 0x6000
	s_waitcnt lgkmcnt(6)
	v_mfma_f32_32x32x16_bf16 v[32:47], v[162:165], v[224:227], v[32:47]
	v_mfma_f32_32x32x16_bf16 v[48:63], v[88:91], v[232:235], v[48:63]
	s_waitcnt lgkmcnt(4)
	v_mfma_f32_32x32x16_bf16 v[32:47], v[176:179], v[228:231], v[32:47]
	v_mfma_f32_32x32x16_bf16 v[48:63], v[92:95], v[236:239], v[48:63]
	ds_read_b64_tr_b16 v[80:81], v146 offset:128
	ds_read_b64_tr_b16 v[82:83], v161 offset:896
	ds_read_b64_tr_b16 v[92:93], v146 offset:6272
	ds_read_b64_tr_b16 v[94:95], v161 offset:7040
	ds_read_b64_tr_b16 v[212:213], v146 offset:12416
	ds_read_b64_tr_b16 v[214:215], v161 offset:13184
	ds_read_b64_tr_b16 v[88:89], v146 offset:18560
	ds_read_b64_tr_b16 v[90:91], v161 offset:19328
	v_add_u32_e32 v146, s14, v147
	v_add_u32_e32 v161, s14, v148
	s_waitcnt lgkmcnt(10)
	v_mfma_f32_32x32x16_bf16 v[32:47], v[204:207], v[232:235], v[32:47]
	ds_read_b64_tr_b16 v[84:85], v166 offset:128
	ds_read_b64_tr_b16 v[86:87], v167 offset:896
	ds_read_b64_tr_b16 v[162:163], v166 offset:6272
	ds_read_b64_tr_b16 v[164:165], v167 offset:7040
	ds_read_b64_tr_b16 v[176:177], v166 offset:12416
	ds_read_b64_tr_b16 v[178:179], v167 offset:13184
	ds_read_b64_tr_b16 v[204:205], v166 offset:18560
	ds_read_b64_tr_b16 v[206:207], v167 offset:19328
	v_add_u32_e32 v166, s14, v149
	v_add_u32_e32 v167, s14, v150
	s_waitcnt lgkmcnt(14)
	v_mfma_f32_32x32x16_bf16 v[0:15], v[80:83], v[224:227], v[0:15]
	s_waitcnt lgkmcnt(6)
	v_mfma_f32_32x32x16_bf16 v[16:31], v[84:87], v[224:227], v[16:31]
	v_mfma_f32_32x32x16_bf16 v[0:15], v[92:95], v[228:231], v[0:15]
	s_waitcnt lgkmcnt(4)
	v_mfma_f32_32x32x16_bf16 v[16:31], v[162:165], v[228:231], v[16:31]
	v_mfma_f32_32x32x16_bf16 v[0:15], v[212:215], v[232:235], v[0:15]
	s_waitcnt lgkmcnt(2)
	v_mfma_f32_32x32x16_bf16 v[16:31], v[176:179], v[232:235], v[16:31]
	v_mfma_f32_32x32x16_bf16 v[32:47], v[208:211], v[236:239], v[32:47]
	v_mfma_f32_32x32x16_bf16 v[0:15], v[88:91], v[236:239], v[0:15]
	s_waitcnt lgkmcnt(0)
	v_mfma_f32_32x32x16_bf16 v[16:31], v[204:207], v[236:239], v[16:31]
	ds_read_b128 v[64:67], v146
	ds_read_b128 v[68:71], v146 offset:12288
	ds_read_b128 v[162:165], v161
	ds_read_b128 v[176:179], v161 offset:12288
	ds_read_b128 v[204:207], v166
	ds_read_b128 v[208:211], v166 offset:12288
	ds_read_b128 v[212:215], v167
	ds_read_b128 v[216:219], v167 offset:12288
	s_waitcnt lgkmcnt(7)
	v_mfma_f32_32x32x16_bf16 v[80:95], v[64:67], v[112:115], 0
	s_waitcnt lgkmcnt(6)
	v_mfma_f32_32x32x16_bf16 v[64:79], v[68:71], v[112:115], 0
	s_waitcnt lgkmcnt(5)
	v_mfma_f32_32x32x16_bf16 v[80:95], v[162:165], v[116:119], v[80:95]
	ds_read_b128 v[162:165], v146 offset:128
	ds_read_b128 v[220:223], v146 offset:12416
	s_waitcnt lgkmcnt(6)
	v_mfma_f32_32x32x16_bf16 v[64:79], v[176:179], v[116:119], v[64:79]
	s_waitcnt lgkmcnt(5)
	v_mfma_f32_32x32x16_bf16 v[80:95], v[204:207], v[120:123], v[80:95]
	ds_read_b128 v[176:179], v161 offset:128
	ds_read_b128 v[204:207], v161 offset:12416
	s_waitcnt lgkmcnt(6)
	v_mfma_f32_32x32x16_bf16 v[64:79], v[208:211], v[120:123], v[64:79]
	s_waitcnt lgkmcnt(5)
	v_mfma_f32_32x32x16_bf16 v[80:95], v[212:215], v[124:127], v[80:95]
	ds_read_b128 v[208:211], v166 offset:128
	ds_read_b128 v[212:215], v166 offset:12416
	s_waitcnt lgkmcnt(6)
	v_mfma_f32_32x32x16_bf16 v[64:79], v[216:219], v[124:127], v[64:79]
	s_waitcnt lgkmcnt(5)
	v_mfma_f32_32x32x16_bf16 v[80:95], v[162:165], v[96:99], v[80:95]
	ds_read_b128 v[162:165], v167 offset:128
	ds_read_b128 v[216:219], v167 offset:12416
	s_waitcnt lgkmcnt(6)
	v_mfma_f32_32x32x16_bf16 v[64:79], v[220:223], v[96:99], v[64:79]
	s_waitcnt lgkmcnt(5)
	v_mfma_f32_32x32x16_bf16 v[80:95], v[176:179], v[100:103], v[80:95]
	ds_read_b128 v[176:179], v146 offset:256
	ds_read_b128 v[220:223], v146 offset:12544
	s_waitcnt lgkmcnt(6)
	v_mfma_f32_32x32x16_bf16 v[64:79], v[204:207], v[100:103], v[64:79]
	s_waitcnt lgkmcnt(5)
	v_mfma_f32_32x32x16_bf16 v[80:95], v[208:211], v[104:107], v[80:95]
	ds_read_b128 v[204:207], v161 offset:256
	ds_read_b128 v[208:211], v161 offset:12544
	s_waitcnt lgkmcnt(6)
	v_mfma_f32_32x32x16_bf16 v[64:79], v[212:215], v[104:107], v[64:79]
	s_waitcnt lgkmcnt(5)
	v_mfma_f32_32x32x16_bf16 v[80:95], v[162:165], v[108:111], v[80:95]
	ds_read_b128 v[162:165], v166 offset:256
	ds_read_b128 v[212:215], v166 offset:12544
	s_waitcnt lgkmcnt(6)
	v_mfma_f32_32x32x16_bf16 v[64:79], v[216:219], v[108:111], v[64:79]
	s_waitcnt lgkmcnt(5)
	v_mfma_f32_32x32x16_bf16 v[80:95], v[176:179], v[128:131], v[80:95]
	ds_read_b128 v[176:179], v167 offset:256
	ds_read_b128 v[216:219], v167 offset:12544
	s_waitcnt lgkmcnt(6)
	v_mfma_f32_32x32x16_bf16 v[64:79], v[220:223], v[128:131], v[64:79]
	s_waitcnt lgkmcnt(5)
	v_mfma_f32_32x32x16_bf16 v[80:95], v[204:207], v[132:135], v[80:95]
	s_waitcnt lgkmcnt(4)
	v_mfma_f32_32x32x16_bf16 v[64:79], v[208:211], v[132:135], v[64:79]
	s_waitcnt lgkmcnt(3)
	v_mfma_f32_32x32x16_bf16 v[80:95], v[162:165], v[136:139], v[80:95]
	s_waitcnt lgkmcnt(2)
	v_mfma_f32_32x32x16_bf16 v[64:79], v[212:215], v[136:139], v[64:79]
	s_waitcnt lgkmcnt(1)
	v_mfma_f32_32x32x16_bf16 v[80:95], v[176:179], v[140:143], v[80:95]
	s_waitcnt lgkmcnt(0)
	v_mfma_f32_32x32x16_bf16 v[64:79], v[216:219], v[140:143], v[64:79]
	s_cmp_le_u32 s7, s44
	s_cbranch_scc1 .Lf_b
	v_add_u32_e32 v146, 59, v156
	v_cmp_gt_u32_e32 vcc, 2.0, v146
	v_add_u32_e32 v146, 27, v156
	s_nop 4
	v_cndmask_b32_e32 v80, v199, v80, vcc
	v_cmp_gt_u32_e32 vcc, 2.0, v146
	v_add_u32_e32 v146, 58, v156
	s_nop 0
	v_cndmask_b32_e32 v64, v199, v64, vcc
	v_cmp_gt_u32_e32 vcc, 2.0, v146
	v_add_u32_e32 v146, 26, v156
	s_nop 0
	v_cndmask_b32_e32 v81, v199, v81, vcc
	v_cmp_gt_u32_e32 vcc, 2.0, v146
	v_add_u32_e32 v146, 57, v156
	s_nop 0
	v_cndmask_b32_e32 v65, v199, v65, vcc
	v_cmp_gt_u32_e32 vcc, 2.0, v146
	v_add_u32_e32 v146, 25, v156
	s_nop 0
	v_cndmask_b32_e32 v82, v199, v82, vcc
	v_cmp_gt_u32_e32 vcc, 2.0, v146
	v_add_u32_e32 v146, 56, v156
	s_nop 0
	v_cndmask_b32_e32 v66, v199, v66, vcc
	v_cmp_gt_u32_e32 vcc, 2.0, v146
	v_add_u32_e32 v146, 24, v156
	s_nop 0
	v_cndmask_b32_e32 v83, v199, v83, vcc
	v_cmp_gt_u32_e32 vcc, 2.0, v146
	v_add_u32_e32 v146, 51, v156
	s_nop 0
	v_cndmask_b32_e32 v67, v199, v67, vcc
	v_cmp_gt_u32_e32 vcc, 2.0, v146
	v_add_u32_e32 v146, 19, v156
	s_nop 0
	v_cndmask_b32_e32 v84, v199, v84, vcc
	v_cmp_gt_u32_e32 vcc, 2.0, v146
	v_add_u32_e32 v146, 50, v156
	s_nop 0
	v_cndmask_b32_e32 v68, v199, v68, vcc
	v_cmp_gt_u32_e32 vcc, 2.0, v146
	v_add_u32_e32 v146, 18, v156
	s_nop 0
	v_cndmask_b32_e32 v85, v199, v85, vcc
	v_cmp_gt_u32_e32 vcc, 2.0, v146
	v_add_u32_e32 v146, 49, v156
	s_nop 0
	v_cndmask_b32_e32 v69, v199, v69, vcc
	v_cmp_gt_u32_e32 vcc, 2.0, v146
	v_add_u32_e32 v146, 17, v156
	s_nop 0
	v_cndmask_b32_e32 v86, v199, v86, vcc
	v_cmp_gt_u32_e32 vcc, 2.0, v146
	v_add_u32_e32 v146, 48, v156
	s_nop 0
	v_cndmask_b32_e32 v70, v199, v70, vcc
	v_cmp_gt_u32_e32 vcc, 2.0, v146
	v_add_u32_e32 v146, 16, v156
	s_nop 0
	v_cndmask_b32_e32 v87, v199, v87, vcc
	v_cmp_gt_u32_e32 vcc, 2.0, v146
	v_add_u32_e32 v146, 43, v156
	s_nop 0
	v_cndmask_b32_e32 v71, v199, v71, vcc
	v_cmp_gt_u32_e32 vcc, 2.0, v146
	v_add_u32_e32 v146, 11, v156
	s_nop 0
	v_cndmask_b32_e32 v88, v199, v88, vcc
	v_cmp_gt_u32_e32 vcc, 2.0, v146
	v_add_u32_e32 v146, 42, v156
	s_nop 0
	v_cndmask_b32_e32 v72, v199, v72, vcc
	v_cmp_gt_u32_e32 vcc, 2.0, v146
	v_add_u32_e32 v146, 10, v156
	s_nop 0
	v_cndmask_b32_e32 v89, v199, v89, vcc
	v_cmp_gt_u32_e32 vcc, 2.0, v146
	v_add_u32_e32 v146, 41, v156
	s_nop 0
	v_cndmask_b32_e32 v73, v199, v73, vcc
	v_cmp_gt_u32_e32 vcc, 2.0, v146
	v_add_u32_e32 v146, 9, v156
	s_nop 0
	v_cndmask_b32_e32 v90, v199, v90, vcc
	v_cmp_gt_u32_e32 vcc, 2.0, v146
	v_add_u32_e32 v146, 40, v156
	s_nop 0
	v_cndmask_b32_e32 v74, v199, v74, vcc
	v_cmp_gt_u32_e32 vcc, 2.0, v146
	v_add_u32_e32 v146, 8, v156
	s_nop 0
	v_cndmask_b32_e32 v91, v199, v91, vcc
	v_cmp_gt_u32_e32 vcc, 2.0, v146
	v_add_u32_e32 v146, 35, v156
	s_nop 0
	v_cndmask_b32_e32 v75, v199, v75, vcc
	v_cmp_gt_u32_e32 vcc, 2.0, v146
	v_add_u32_e32 v146, 3, v156
	s_nop 0
	v_cndmask_b32_e32 v92, v199, v92, vcc
	v_cmp_gt_u32_e32 vcc, 2.0, v146
	v_add_u32_e32 v146, 34, v156
	s_nop 0
	v_cndmask_b32_e32 v76, v199, v76, vcc
	v_cmp_gt_u32_e32 vcc, 2.0, v146
	v_add_u32_e32 v146, 2, v156
	s_nop 0
	v_cndmask_b32_e32 v93, v199, v93, vcc
	v_cmp_gt_u32_e32 vcc, 2.0, v146
	v_add_u32_e32 v146, 33, v156
	s_nop 0
	v_cndmask_b32_e32 v77, v199, v77, vcc
	v_cmp_gt_u32_e32 vcc, 2.0, v146
	v_add_u32_e32 v146, 1, v156
	s_nop 0
	v_cndmask_b32_e32 v94, v199, v94, vcc
	v_cmp_gt_u32_e32 vcc, 2.0, v146
	v_add_u32_e32 v146, 32, v156
	s_nop 0
	v_cndmask_b32_e32 v78, v199, v78, vcc
	v_cmp_gt_u32_e32 vcc, 2.0, v146
	s_nop 1
	v_cndmask_b32_e32 v95, v199, v95, vcc
	v_cmp_gt_u32_e32 vcc, 2.0, v156
	s_nop 1
	v_cndmask_b32_e32 v79, v199, v79, vcc
.Lf_b:
	s_nop 9
	v_exp_f32_e32 v240, v80
	v_exp_f32_e32 v241, v81
	v_exp_f32_e32 v242, v82
	v_exp_f32_e32 v243, v83
	v_exp_f32_e32 v244, v84
	v_exp_f32_e32 v245, v85
	v_exp_f32_e32 v246, v86
	v_exp_f32_e32 v247, v87
	v_add_f32_e32 v159, v240, v241
	v_add_f32_e32 v159, v242, v159
	v_add_f32_e32 v159, v243, v159
	v_add_f32_e32 v159, v244, v159
	v_add_f32_e32 v159, v245, v159
	v_add_f32_e32 v159, v246, v159
	v_add_f32_e32 v159, v247, v159
	v_cvt_pk_bf16_f32 v224, v240, v241
	v_cvt_pk_bf16_f32 v225, v244, v245
	v_cvt_pk_bf16_f32 v226, v242, v243
	v_cvt_pk_bf16_f32 v227, v246, v247
	v_exp_f32_e32 v240, v88
	v_exp_f32_e32 v241, v89
	v_exp_f32_e32 v242, v90
	v_exp_f32_e32 v243, v91
	v_exp_f32_e32 v244, v92
	v_exp_f32_e32 v245, v93
	v_exp_f32_e32 v246, v94
	v_exp_f32_e32 v247, v95
	v_add_f32_e32 v159, v240, v159
	v_add_f32_e32 v159, v241, v159
	v_add_f32_e32 v159, v242, v159
	v_add_f32_e32 v159, v243, v159
	v_add_f32_e32 v159, v244, v159
	v_add_f32_e32 v159, v245, v159
	v_add_f32_e32 v159, v246, v159
	v_add_f32_e32 v159, v247, v159
	v_cvt_pk_bf16_f32 v228, v240, v241
	v_cvt_pk_bf16_f32 v229, v244, v245
	v_cvt_pk_bf16_f32 v230, v242, v243
	v_cvt_pk_bf16_f32 v231, v246, v247
	v_exp_f32_e32 v240, v64
	v_exp_f32_e32 v241, v65
	v_exp_f32_e32 v242, v66
	v_exp_f32_e32 v243, v67
	v_exp_f32_e32 v244, v68
	v_exp_f32_e32 v245, v69
	v_exp_f32_e32 v246, v70
	v_exp_f32_e32 v247, v71
	v_add_f32_e32 v159, v240, v159
	v_add_f32_e32 v159, v241, v159
	v_add_f32_e32 v159, v242, v159
	v_add_f32_e32 v159, v243, v159
	v_add_f32_e32 v159, v244, v159
	v_add_f32_e32 v159, v245, v159
	v_add_f32_e32 v159, v246, v159
	v_add_f32_e32 v159, v247, v159
	v_cvt_pk_bf16_f32 v232, v240, v241
	v_cvt_pk_bf16_f32 v233, v244, v245
	v_cvt_pk_bf16_f32 v234, v242, v243
	v_cvt_pk_bf16_f32 v235, v246, v247
	v_exp_f32_e32 v240, v72
	v_exp_f32_e32 v241, v73
	v_exp_f32_e32 v242, v74
	v_exp_f32_e32 v243, v75
	v_exp_f32_e32 v244, v76
	v_exp_f32_e32 v245, v77
	v_exp_f32_e32 v246, v78
	v_exp_f32_e32 v247, v79
	v_add_f32_e32 v159, v240, v159
	v_add_f32_e32 v159, v241, v159
	v_add_f32_e32 v159, v242, v159
	v_add_f32_e32 v159, v243, v159
	v_add_f32_e32 v159, v244, v159
	v_add_f32_e32 v159, v245, v159
	v_add_f32_e32 v159, v246, v159
	v_add_f32_e32 v159, v247, v159
	v_cvt_pk_bf16_f32 v236, v240, v241
	v_cvt_pk_bf16_f32 v237, v244, v245
	v_cvt_pk_bf16_f32 v238, v242, v243
	v_cvt_pk_bf16_f32 v239, v246, v247
	v_cmp_gt_f32_e32 vcc, 0x7149f2ca, v159
	s_cmp_eq_u64 vcc, exec
	s_cbranch_scc0 .Lf_b_fail
	v_add_f32_e32 v158, v158, v159
	v_add_u32_e32 v209, s14, v151
	v_add_u32_e32 v210, s14, v152
	ds_read_b64_tr_b16 v[64:65], v209
	ds_read_b64_tr_b16 v[66:67], v210 offset:768
	s_waitcnt lgkmcnt(0)
	v_mfma_f32_32x32x16_bf16 v[48:63], v[64:67], v[224:227], v[48:63]
	ds_read_b64_tr_b16 v[68:69], v209 offset:6144
	ds_read_b64_tr_b16 v[70:71], v210 offset:6912
	ds_read_b64_tr_b16 v[64:65], v209 offset:12288
	ds_read_b64_tr_b16 v[66:67], v210 offset:13056
	s_waitcnt lgkmcnt(2)
	v_mfma_f32_32x32x16_bf16 v[48:63], v[68:71], v[228:231], v[48:63]
	v_add_u32_e32 v213, s14, v153
	ds_read_b64_tr_b16 v[80:81], v209 offset:18432
	ds_read_b64_tr_b16 v[82:83], v210 offset:19200
	s_waitcnt lgkmcnt(2)
	v_mfma_f32_32x32x16_bf16 v[48:63], v[64:67], v[232:235], v[48:63]
	ds_read_b64_tr_b16 v[84:85], v213
	v_add_u32_e32 v214, s14, v154
	s_waitcnt lgkmcnt(1)
	v_mfma_f32_32x32x16_bf16 v[48:63], v[80:83], v[236:239], v[48:63]
	ds_read_b64_tr_b16 v[86:87], v214 offset:768
	ds_read_b64_tr_b16 v[80:81], v213 offset:6144
	s_addk_i32 s12, 0x1000
	s_add_i32 s11, s11, 4
	s_add_i32 s10, s10, 2
	s_addk_i32 s7, 0x80
	v_add_u32_e32 v155, 32, v155
	s_waitcnt lgkmcnt(1)
	v_mfma_f32_32x32x16_bf16 v[32:47], v[84:87], v[224:227], v[32:47]
	ds_read_b64_tr_b16 v[82:83], v214 offset:6912
	ds_read_b64_tr_b16 v[84:85], v213 offset:12288
	s_cmp_ge_u32 s13, s9
	v_add_u32_e32 v156, 0xffffff80, v156
	s_waitcnt lgkmcnt(1)
	v_mfma_f32_32x32x16_bf16 v[32:47], v[80:83], v[228:231], v[32:47]
	ds_read_b64_tr_b16 v[86:87], v214 offset:13056
	ds_read_b64_tr_b16 v[80:81], v213 offset:18432
	s_waitcnt lgkmcnt(1)
	v_mfma_f32_32x32x16_bf16 v[32:47], v[84:87], v[232:235], v[32:47]
	ds_read_b64_tr_b16 v[82:83], v214 offset:19200
	ds_read_b64_tr_b16 v[84:85], v209 offset:128
	ds_read_b64_tr_b16 v[86:87], v210 offset:896
	s_waitcnt lgkmcnt(0)
	v_mfma_f32_32x32x16_bf16 v[0:15], v[84:87], v[224:227], v[0:15]
	v_mfma_f32_32x32x16_bf16 v[32:47], v[80:83], v[236:239], v[32:47]
	ds_read_b64_tr_b16 v[80:81], v209 offset:6272
	ds_read_b64_tr_b16 v[82:83], v210 offset:7040
	ds_read_b64_tr_b16 v[84:85], v209 offset:12416
	ds_read_b64_tr_b16 v[86:87], v210 offset:13184
	s_waitcnt lgkmcnt(2)
	v_mfma_f32_32x32x16_bf16 v[0:15], v[80:83], v[228:231], v[0:15]
	ds_read_b64_tr_b16 v[80:81], v209 offset:18560
	ds_read_b64_tr_b16 v[82:83], v210 offset:19328
	s_waitcnt lgkmcnt(2)
	v_mfma_f32_32x32x16_bf16 v[0:15], v[84:87], v[232:235], v[0:15]
	ds_read_b64_tr_b16 v[84:85], v213 offset:128
	ds_read_b64_tr_b16 v[86:87], v214 offset:896
	s_waitcnt lgkmcnt(2)
	v_mfma_f32_32x32x16_bf16 v[0:15], v[80:83], v[236:239], v[0:15]
	ds_read_b64_tr_b16 v[80:81], v213 offset:6272
	ds_read_b64_tr_b16 v[82:83], v214 offset:7040
	s_waitcnt lgkmcnt(2)
	v_mfma_f32_32x32x16_bf16 v[16:31], v[84:87], v[224:227], v[16:31]
	ds_read_b64_tr_b16 v[72:73], v213 offset:12416
	ds_read_b64_tr_b16 v[74:75], v214 offset:13184
	s_waitcnt lgkmcnt(2)
	v_mfma_f32_32x32x16_bf16 v[16:31], v[80:83], v[228:231], v[16:31]
	ds_read_b64_tr_b16 v[76:77], v213 offset:18560
	ds_read_b64_tr_b16 v[78:79], v214 offset:19328
	s_waitcnt vmcnt(0)
	s_waitcnt lgkmcnt(2)
	v_mfma_f32_32x32x16_bf16 v[16:31], v[72:75], v[232:235], v[16:31]
	s_waitcnt lgkmcnt(0)
	v_mfma_f32_32x32x16_bf16 v[16:31], v[76:79], v[236:239], v[16:31]
	s_barrier
	s_cbranch_scc1 .LBB0_1250
	s_branch .LBB0_1238
.Lf_a_fail:
	s_mov_b32 s101, 0
	v_mov_b32_e32 v160, v158
	s_nop 1
	v_permlane32_swap_b32_e32 v158, v160
	v_add_f32_e32 v158, v158, v160
	s_branch .Lslow_a
.Lf_b_fail:
	s_mov_b32 s101, 0
	v_mov_b32_e32 v160, v158
	s_nop 1
	v_permlane32_swap_b32_e32 v158, v160
	v_add_f32_e32 v158, v158, v160
	v_mov_b32_e32 v159, 0
	v_mov_b32_e32 v160, 0
	v_mov_b32_e32 v144, 1.0
	s_branch .LBB0_1248
.LBB0_1250:
	s_cmp_eq_u32 s101, 0
	s_cbranch_scc1 .Lf_end
	v_mov_b32_e32 v160, v158
	s_nop 1
	v_permlane32_swap_b32_e32 v158, v160
	v_add_f32_e32 v158, v158, v160

.LBB0_1380:
	v_cmp_gt_u32_e64 s[4:5], 32, v192
	s_and_saveexec_b64 s[8:9], s[4:5]
	ds_write_b32 v187, v154 offset:128
	s_or_b64 exec, exec, s[8:9]
	v_add_u32_e32 v83, s24, v191
	ds_read_b128 v[78:81], v83 offset:128
	ds_read_b128 v[74:77], v83 offset:160
	s_ashr_i32 s16, s16, 8
	s_ashr_i32 s17, s16, 31
	s_lshl_b64 s[8:9], s[16:17], 24
	s_add_u32 s8, s20, s8
	s_addc_u32 s9, s21, s9
	s_lshl_b32 s17, s35, 17
	s_waitcnt lgkmcnt(1)
	v_rcp_f32_e32 v78, v78
	s_add_u32 s8, s8, s17
	ds_read_b128 v[70:73], v83 offset:192
	ds_read_b128 v[66:69], v83 offset:224
	s_addc_u32 s9, s9, 0
	s_lshl_b32 s17, s18, 7
	s_add_u32 s8, s8, s17
	s_waitcnt vmcnt(0)
	v_and_b32_e32 v0, 1, v188
	s_addc_u32 s9, s9, 0
	v_cmp_eq_u32_e32 vcc, 0, v0
	v_lshl_or_b32 v0, v189, 12, v190
	v_readlane_b32 s99, v251, 5
	s_lshr_b32 s99, s99, 6
	s_lshl_b32 s99, s99, 12
	s_add_i32 s99, s99, 0x14000
	v_mbcnt_lo_u32_b32 v249, -1, 0
	v_mbcnt_hi_u32_b32 v249, -1, v249
	v_lshrrev_b32_e32 v252, 5, v249
	v_and_b32_e32 v249, 31, v249
	v_lshlrev_b32_e32 v249, 1, v249
	v_lshl_add_u32 v249, v252, 9, v249
	v_add_u32_e32 v249, s99, v249
	v_mul_f32_e32 v84, v50, v78
	s_and_b32 s9, s9, 0xffff
	v_lshlrev_b32_e32 v50, 1, v0
	v_mov_b32_dpp v85, v84 quad_perm:[1,0,3,2] row_mask:0xf bank_mask:0xf bound_ctrl:1
	s_and_saveexec_b64 s[18:19], vcc
	s_cbranch_execz .LBB0_1384
	v_cvt_pk_bf16_f32 v84, v84, v85
	ds_write_b32 v249, v84
.LBB0_1384:
	s_or_b64 exec, exec, s[18:19]
	v_mul_f32_e32 v34, v34, v78
	s_nop 1
	v_mov_b32_dpp v78, v34 quad_perm:[1,0,3,2] row_mask:0xf bank_mask:0xf bound_ctrl:1
	s_and_saveexec_b64 s[18:19], vcc
	s_cbranch_execz .LBB0_1386
	v_cvt_pk_bf16_f32 v34, v34, v78
	ds_write_b32 v249, v34 offset:64
.LBB0_1386:
	s_or_b64 exec, exec, s[18:19]
	v_rcp_f32_e32 v50, v79
	v_or_b32_e32 v34, 0x400, v0
	v_lshlrev_b32_e32 v34, 1, v34
	v_mul_f32_e32 v51, v51, v50
	s_nop 1
	v_mov_b32_dpp v78, v51 quad_perm:[1,0,3,2] row_mask:0xf bank_mask:0xf bound_ctrl:1
	s_and_saveexec_b64 s[18:19], vcc
	s_cbranch_execz .LBB0_1388
	v_cvt_pk_bf16_f32 v51, v51, v78
	ds_write_b32 v249, v51 offset:128
.LBB0_1388:
	s_or_b64 exec, exec, s[18:19]
	v_mul_f32_e32 v35, v35, v50
	s_nop 1
	v_mov_b32_dpp v50, v35 quad_perm:[1,0,3,2] row_mask:0xf bank_mask:0xf bound_ctrl:1
	s_and_saveexec_b64 s[18:19], vcc
	s_cbranch_execz .LBB0_1390
	v_cvt_pk_bf16_f32 v35, v35, v50
	ds_write_b32 v249, v35 offset:192
.LBB0_1390:
	s_or_b64 exec, exec, s[18:19]
	v_rcp_f32_e32 v35, v80
	v_or_b32_e32 v34, 0x800, v0
	v_lshlrev_b32_e32 v34, 1, v34
	v_mul_f32_e32 v50, v52, v35
	s_nop 1
	v_mov_b32_dpp v51, v50 quad_perm:[1,0,3,2] row_mask:0xf bank_mask:0xf bound_ctrl:1
	s_and_saveexec_b64 s[18:19], vcc
	s_cbranch_execz .LBB0_1392
	v_cvt_pk_bf16_f32 v50, v50, v51
	ds_write_b32 v249, v50 offset:256
.LBB0_1392:
	s_or_b64 exec, exec, s[18:19]
	v_mul_f32_e32 v35, v36, v35
	s_nop 1
	v_mov_b32_dpp v36, v35 quad_perm:[1,0,3,2] row_mask:0xf bank_mask:0xf bound_ctrl:1
	s_and_saveexec_b64 s[18:19], vcc
	s_cbranch_execz .LBB0_1394
	v_cvt_pk_bf16_f32 v35, v35, v36
	ds_write_b32 v249, v35 offset:320
.LBB0_1394:
	s_or_b64 exec, exec, s[18:19]
	v_rcp_f32_e32 v35, v81
	v_or_b32_e32 v34, 0xc00, v0
	v_lshlrev_b32_e32 v34, 1, v34
	v_mul_f32_e32 v36, v53, v35
	s_nop 1
	v_mov_b32_dpp v50, v36 quad_perm:[1,0,3,2] row_mask:0xf bank_mask:0xf bound_ctrl:1
	s_and_saveexec_b64 s[18:19], vcc
	s_cbranch_execz .LBB0_1396
	v_cvt_pk_bf16_f32 v36, v36, v50
	ds_write_b32 v249, v36 offset:384
.LBB0_1396:
	s_or_b64 exec, exec, s[18:19]
	v_mul_f32_e32 v35, v37, v35
	s_nop 1
	v_mov_b32_dpp v36, v35 quad_perm:[1,0,3,2] row_mask:0xf bank_mask:0xf bound_ctrl:1
	s_and_saveexec_b64 s[18:19], vcc
	s_cbranch_execz .LBB0_1398
	v_cvt_pk_bf16_f32 v35, v35, v36
	ds_write_b32 v249, v35 offset:448
.LBB0_1398:
	s_or_b64 exec, exec, s[18:19]
	s_waitcnt lgkmcnt(2)
	v_rcp_f32_e32 v35, v74
	v_or_b32_e32 v34, 0x2000, v0
	v_lshlrev_b32_e32 v34, 1, v34
	v_mul_f32_e32 v36, v54, v35
	s_nop 1
	v_mov_b32_dpp v37, v36 quad_perm:[1,0,3,2] row_mask:0xf bank_mask:0xf bound_ctrl:1
	s_and_saveexec_b64 s[18:19], vcc
	s_cbranch_execz .LBB0_1400
	v_cvt_pk_bf16_f32 v36, v36, v37
	ds_write_b32 v249, v36 offset:1024
.LBB0_1400:
	s_or_b64 exec, exec, s[18:19]
	v_mul_f32_e32 v35, v38, v35
	s_nop 1
	v_mov_b32_dpp v36, v35 quad_perm:[1,0,3,2] row_mask:0xf bank_mask:0xf bound_ctrl:1
	s_and_saveexec_b64 s[18:19], vcc
	s_cbranch_execz .LBB0_1402
	v_cvt_pk_bf16_f32 v35, v35, v36
	ds_write_b32 v249, v35 offset:1088
.LBB0_1402:
	s_or_b64 exec, exec, s[18:19]
	v_rcp_f32_e32 v35, v75
	v_or_b32_e32 v34, 0x2400, v0
	v_lshlrev_b32_e32 v34, 1, v34
	v_mul_f32_e32 v36, v55, v35
	s_nop 1
	v_mov_b32_dpp v37, v36 quad_perm:[1,0,3,2] row_mask:0xf bank_mask:0xf bound_ctrl:1
	s_and_saveexec_b64 s[18:19], vcc
	s_cbranch_execz .LBB0_1404
	v_cvt_pk_bf16_f32 v36, v36, v37
	ds_write_b32 v249, v36 offset:1152
.LBB0_1404:
	s_or_b64 exec, exec, s[18:19]
	v_mul_f32_e32 v35, v39, v35
	s_nop 1
	v_mov_b32_dpp v36, v35 quad_perm:[1,0,3,2] row_mask:0xf bank_mask:0xf bound_ctrl:1
	s_and_saveexec_b64 s[18:19], vcc
	s_cbranch_execz .LBB0_1406
	v_cvt_pk_bf16_f32 v35, v35, v36
	ds_write_b32 v249, v35 offset:1216
.LBB0_1406:
	s_or_b64 exec, exec, s[18:19]
	v_rcp_f32_e32 v35, v76
	v_or_b32_e32 v34, 0x2800, v0
	v_lshlrev_b32_e32 v34, 1, v34
	v_mul_f32_e32 v36, v56, v35
	s_nop 1
	v_mov_b32_dpp v37, v36 quad_perm:[1,0,3,2] row_mask:0xf bank_mask:0xf bound_ctrl:1
	s_and_saveexec_b64 s[18:19], vcc
	s_cbranch_execz .LBB0_1408
	v_cvt_pk_bf16_f32 v36, v36, v37
	ds_write_b32 v249, v36 offset:1280
.LBB0_1408:
	s_or_b64 exec, exec, s[18:19]
	v_mul_f32_e32 v35, v40, v35
	s_nop 1
	v_mov_b32_dpp v36, v35 quad_perm:[1,0,3,2] row_mask:0xf bank_mask:0xf bound_ctrl:1
	s_and_saveexec_b64 s[18:19], vcc
	s_cbranch_execz .LBB0_1410
	v_cvt_pk_bf16_f32 v35, v35, v36
	ds_write_b32 v249, v35 offset:1344
.LBB0_1410:
	s_or_b64 exec, exec, s[18:19]
	v_rcp_f32_e32 v35, v77
	v_or_b32_e32 v34, 0x2c00, v0
	v_lshlrev_b32_e32 v34, 1, v34
	v_mul_f32_e32 v36, v57, v35
	s_nop 1
	v_mov_b32_dpp v37, v36 quad_perm:[1,0,3,2] row_mask:0xf bank_mask:0xf bound_ctrl:1
	s_and_saveexec_b64 s[18:19], vcc
	s_cbranch_execz .LBB0_1412
	v_cvt_pk_bf16_f32 v36, v36, v37
	ds_write_b32 v249, v36 offset:1408
.LBB0_1412:
	s_or_b64 exec, exec, s[18:19]
	v_mul_f32_e32 v35, v41, v35
	s_nop 1
	v_mov_b32_dpp v36, v35 quad_perm:[1,0,3,2] row_mask:0xf bank_mask:0xf bound_ctrl:1
	s_and_saveexec_b64 s[18:19], vcc
	s_cbranch_execz .LBB0_1414
	v_cvt_pk_bf16_f32 v35, v35, v36
	ds_write_b32 v249, v35 offset:1472
.LBB0_1414:
	s_or_b64 exec, exec, s[18:19]
	s_waitcnt lgkmcnt(1)
	v_rcp_f32_e32 v35, v70
	v_or_b32_e32 v34, 0x4000, v0
	v_lshlrev_b32_e32 v34, 1, v34
	v_mul_f32_e32 v36, v58, v35
	s_nop 1
	v_mov_b32_dpp v37, v36 quad_perm:[1,0,3,2] row_mask:0xf bank_mask:0xf bound_ctrl:1
	s_and_saveexec_b64 s[18:19], vcc
	s_cbranch_execz .LBB0_1416
	v_cvt_pk_bf16_f32 v36, v36, v37
	ds_write_b32 v249, v36 offset:2048
.LBB0_1416:
	s_or_b64 exec, exec, s[18:19]
	v_mul_f32_e32 v35, v42, v35
	s_nop 1
	v_mov_b32_dpp v36, v35 quad_perm:[1,0,3,2] row_mask:0xf bank_mask:0xf bound_ctrl:1
	s_and_saveexec_b64 s[18:19], vcc
	s_cbranch_execz .LBB0_1418
	v_cvt_pk_bf16_f32 v35, v35, v36
	ds_write_b32 v249, v35 offset:2112
.LBB0_1418:
	s_or_b64 exec, exec, s[18:19]
	v_rcp_f32_e32 v35, v71
	v_or_b32_e32 v34, 0x4400, v0
	v_lshlrev_b32_e32 v34, 1, v34
	v_mul_f32_e32 v36, v59, v35
	s_nop 1
	v_mov_b32_dpp v37, v36 quad_perm:[1,0,3,2] row_mask:0xf bank_mask:0xf bound_ctrl:1
	s_and_saveexec_b64 s[18:19], vcc
	s_cbranch_execz .LBB0_1420
	v_cvt_pk_bf16_f32 v36, v36, v37
	ds_write_b32 v249, v36 offset:2176
.LBB0_1420:
	s_or_b64 exec, exec, s[18:19]
	v_mul_f32_e32 v35, v43, v35
	s_nop 1
	v_mov_b32_dpp v36, v35 quad_perm:[1,0,3,2] row_mask:0xf bank_mask:0xf bound_ctrl:1
	s_and_saveexec_b64 s[18:19], vcc
	s_cbranch_execz .LBB0_1422
	v_cvt_pk_bf16_f32 v35, v35, v36
	ds_write_b32 v249, v35 offset:2240
.LBB0_1422:
	s_or_b64 exec, exec, s[18:19]
	v_rcp_f32_e32 v35, v72
	v_or_b32_e32 v34, 0x4800, v0
	v_lshlrev_b32_e32 v34, 1, v34
	v_mul_f32_e32 v36, v60, v35
	s_nop 1
	v_mov_b32_dpp v37, v36 quad_perm:[1,0,3,2] row_mask:0xf bank_mask:0xf bound_ctrl:1
	s_and_saveexec_b64 s[18:19], vcc
	s_cbranch_execz .LBB0_1424
	v_cvt_pk_bf16_f32 v36, v36, v37
	ds_write_b32 v249, v36 offset:2304
.LBB0_1424:
	s_or_b64 exec, exec, s[18:19]
	v_mul_f32_e32 v35, v44, v35
	s_nop 1
	v_mov_b32_dpp v36, v35 quad_perm:[1,0,3,2] row_mask:0xf bank_mask:0xf bound_ctrl:1
	s_and_saveexec_b64 s[18:19], vcc
	s_cbranch_execz .LBB0_1426
	v_cvt_pk_bf16_f32 v35, v35, v36
	ds_write_b32 v249, v35 offset:2368
.LBB0_1426:
	s_or_b64 exec, exec, s[18:19]
	v_rcp_f32_e32 v35, v73
	v_or_b32_e32 v34, 0x4c00, v0
	v_lshlrev_b32_e32 v34, 1, v34
	v_mul_f32_e32 v36, v61, v35
	s_nop 1
	v_mov_b32_dpp v37, v36 quad_perm:[1,0,3,2] row_mask:0xf bank_mask:0xf bound_ctrl:1
	s_and_saveexec_b64 s[18:19], vcc
	s_cbranch_execz .LBB0_1428
	v_cvt_pk_bf16_f32 v36, v36, v37
	ds_write_b32 v249, v36 offset:2432
.LBB0_1428:
	s_or_b64 exec, exec, s[18:19]
	v_mul_f32_e32 v35, v45, v35
	s_nop 1
	v_mov_b32_dpp v36, v35 quad_perm:[1,0,3,2] row_mask:0xf bank_mask:0xf bound_ctrl:1
	s_and_saveexec_b64 s[18:19], vcc
	s_cbranch_execz .LBB0_1430
	v_cvt_pk_bf16_f32 v35, v35, v36
	ds_write_b32 v249, v35 offset:2496
.LBB0_1430:
	s_or_b64 exec, exec, s[18:19]
	s_waitcnt lgkmcnt(0)
	v_rcp_f32_e32 v35, v66
	v_or_b32_e32 v34, 0x6000, v0
	v_lshlrev_b32_e32 v34, 1, v34
	v_mul_f32_e32 v36, v62, v35
	s_nop 1
	v_mov_b32_dpp v37, v36 quad_perm:[1,0,3,2] row_mask:0xf bank_mask:0xf bound_ctrl:1
	s_and_saveexec_b64 s[18:19], vcc
	s_cbranch_execz .LBB0_1432
	v_cvt_pk_bf16_f32 v36, v36, v37
	ds_write_b32 v249, v36 offset:3072
.LBB0_1432:
	s_or_b64 exec, exec, s[18:19]
	v_mul_f32_e32 v35, v46, v35
	s_nop 1
	v_mov_b32_dpp v36, v35 quad_perm:[1,0,3,2] row_mask:0xf bank_mask:0xf bound_ctrl:1
	s_and_saveexec_b64 s[18:19], vcc
	s_cbranch_execz .LBB0_1434
	v_cvt_pk_bf16_f32 v35, v35, v36
	ds_write_b32 v249, v35 offset:3136
.LBB0_1434:
	s_or_b64 exec, exec, s[18:19]
	v_rcp_f32_e32 v35, v67
	v_or_b32_e32 v34, 0x6400, v0
	v_lshlrev_b32_e32 v34, 1, v34
	v_mul_f32_e32 v36, v63, v35
	s_nop 1
	v_mov_b32_dpp v37, v36 quad_perm:[1,0,3,2] row_mask:0xf bank_mask:0xf bound_ctrl:1
	s_and_saveexec_b64 s[18:19], vcc
	s_cbranch_execz .LBB0_1436
	v_cvt_pk_bf16_f32 v36, v36, v37
	ds_write_b32 v249, v36 offset:3200
.LBB0_1436:
	s_or_b64 exec, exec, s[18:19]
	v_mul_f32_e32 v35, v47, v35
	s_nop 1
	v_mov_b32_dpp v36, v35 quad_perm:[1,0,3,2] row_mask:0xf bank_mask:0xf bound_ctrl:1
	s_and_saveexec_b64 s[18:19], vcc
	s_cbranch_execz .LBB0_1438
	v_cvt_pk_bf16_f32 v35, v35, v36
	ds_write_b32 v249, v35 offset:3264
.LBB0_1438:
	s_or_b64 exec, exec, s[18:19]
	v_rcp_f32_e32 v35, v68
	v_or_b32_e32 v34, 0x6800, v0
	v_lshlrev_b32_e32 v34, 1, v34
	v_mul_f32_e32 v36, v64, v35
	s_nop 1
	v_mov_b32_dpp v37, v36 quad_perm:[1,0,3,2] row_mask:0xf bank_mask:0xf bound_ctrl:1
	s_and_saveexec_b64 s[18:19], vcc
	s_cbranch_execz .LBB0_1440
	v_cvt_pk_bf16_f32 v36, v36, v37
	ds_write_b32 v249, v36 offset:3328
.LBB0_1440:
	s_or_b64 exec, exec, s[18:19]
	v_mul_f32_e32 v35, v48, v35
	s_nop 1
	v_mov_b32_dpp v36, v35 quad_perm:[1,0,3,2] row_mask:0xf bank_mask:0xf bound_ctrl:1
	s_and_saveexec_b64 s[18:19], vcc
	s_cbranch_execz .LBB0_1442
	v_cvt_pk_bf16_f32 v35, v35, v36
	ds_write_b32 v249, v35 offset:3392
.LBB0_1442:
	s_or_b64 exec, exec, s[18:19]
	v_rcp_f32_e32 v35, v69
	v_or_b32_e32 v34, 0x6c00, v0
	v_lshlrev_b32_e32 v34, 1, v34
	v_mul_f32_e32 v36, v65, v35
	s_nop 1
	v_mov_b32_dpp v37, v36 quad_perm:[1,0,3,2] row_mask:0xf bank_mask:0xf bound_ctrl:1
	s_and_saveexec_b64 s[18:19], vcc
	s_cbranch_execz .LBB0_1444
	v_cvt_pk_bf16_f32 v36, v36, v37
	ds_write_b32 v249, v36 offset:3456
.LBB0_1444:
	s_or_b64 exec, exec, s[18:19]
	v_mul_f32_e32 v35, v49, v35
	s_nop 1
	v_mov_b32_dpp v36, v35 quad_perm:[1,0,3,2] row_mask:0xf bank_mask:0xf bound_ctrl:1
	s_and_saveexec_b64 s[18:19], vcc
	s_cbranch_execz .LBB0_1446
	v_cvt_pk_bf16_f32 v35, v35, v36
	ds_write_b32 v249, v35 offset:3520
.LBB0_1446:
	s_or_b64 exec, exec, s[18:19]
	s_waitcnt lgkmcnt(0)
	v_mbcnt_lo_u32_b32 v249, -1, 0
	v_mbcnt_hi_u32_b32 v249, -1, v249
	v_and_b32_e32 v252, 7, v249
	v_lshrrev_b32_e32 v249, 3, v249
	v_lshlrev_b32_e32 v252, 4, v252
	v_lshl_or_b32 v249, v249, 11, v252
	v_mbcnt_lo_u32_b32 v252, -1, 0
	v_mbcnt_hi_u32_b32 v252, -1, v252
	v_lshl_add_u32 v252, v252, 4, s99
	ds_read_b128 v[252:255], v252
	s_mov_b32 s100, 0x0
	s_waitcnt lgkmcnt(0)
	buffer_store_dwordx4 v[252:255], v249, s[8:11], s100 offen sc1
	s_nop 1
	v_mbcnt_lo_u32_b32 v252, -1, 0
	v_mbcnt_hi_u32_b32 v252, -1, v252
	v_lshl_add_u32 v252, v252, 4, s99
	ds_read_b128 v[252:255], v252 offset:1024
	s_mov_b32 s100, 0x4000
	s_waitcnt lgkmcnt(0)
	buffer_store_dwordx4 v[252:255], v249, s[8:11], s100 offen sc1
	s_nop 1
	v_mbcnt_lo_u32_b32 v252, -1, 0
	v_mbcnt_hi_u32_b32 v252, -1, v252
	v_lshl_add_u32 v252, v252, 4, s99
	ds_read_b128 v[252:255], v252 offset:2048
	s_mov_b32 s100, 0x8000
	s_waitcnt lgkmcnt(0)
	buffer_store_dwordx4 v[252:255], v249, s[8:11], s100 offen sc1
	s_nop 1
	v_mbcnt_lo_u32_b32 v252, -1, 0
	v_mbcnt_hi_u32_b32 v252, -1, v252
	v_lshl_add_u32 v252, v252, 4, s99
	ds_read_b128 v[252:255], v252 offset:3072
	s_mov_b32 s100, 0xc000
	s_waitcnt lgkmcnt(0)
	buffer_store_dwordx4 v[252:255], v249, s[8:11], s100 offen sc1
	s_nop 1
	v_mbcnt_lo_u32_b32 v249, -1, 0
	v_mbcnt_hi_u32_b32 v249, -1, v249
	v_lshrrev_b32_e32 v252, 5, v249
	v_and_b32_e32 v249, 31, v249
	v_lshlrev_b32_e32 v249, 1, v249
	v_lshl_add_u32 v249, v252, 9, v249
	v_add_u32_e32 v249, s99, v249
	s_waitcnt lgkmcnt(0)
	s_and_saveexec_b64 s[18:19], s[4:5]
	ds_write_b32 v187, v82 offset:128
	s_or_b64 exec, exec, s[18:19]
	ds_read_b128 v[46:49], v83 offset:128
	ds_read_b128 v[42:45], v83 offset:160
	ds_read_b128 v[38:41], v83 offset:192
	ds_read_b128 v[34:37], v83 offset:224
	v_or_b32_e32 v52, 0x8000, v0
	s_waitcnt lgkmcnt(3)
	v_rcp_f32_e32 v46, v46
	s_nop 0
	v_mul_f32_e32 v50, v18, v46
	s_nop 1
	v_mov_b32_dpp v51, v50 quad_perm:[1,0,3,2] row_mask:0xf bank_mask:0xf bound_ctrl:1
	v_lshlrev_b32_e32 v18, 1, v52
	s_and_saveexec_b64 s[4:5], vcc
	s_cbranch_execz .LBB0_1450
	v_cvt_pk_bf16_f32 v50, v50, v51
	ds_write_b32 v249, v50

.LBB0_1512:
	s_or_b64 exec, exec, s[4:5]
	s_waitcnt lgkmcnt(0)
	v_mbcnt_lo_u32_b32 v249, -1, 0
	v_mbcnt_hi_u32_b32 v249, -1, v249
	v_and_b32_e32 v252, 7, v249
	v_lshrrev_b32_e32 v249, 3, v249
	v_lshlrev_b32_e32 v252, 4, v252
	v_lshl_or_b32 v249, v249, 11, v252
	v_mbcnt_lo_u32_b32 v252, -1, 0
	v_mbcnt_hi_u32_b32 v252, -1, v252
	v_lshl_add_u32 v252, v252, 4, s99
	ds_read_b128 v[252:255], v252
	s_mov_b32 s100, 0x10000
	s_waitcnt lgkmcnt(0)
	buffer_store_dwordx4 v[252:255], v249, s[8:11], s100 offen sc1
	s_nop 1
	v_mbcnt_lo_u32_b32 v252, -1, 0
	v_mbcnt_hi_u32_b32 v252, -1, v252
	v_lshl_add_u32 v252, v252, 4, s99
	ds_read_b128 v[252:255], v252 offset:1024
	s_mov_b32 s100, 0x14000
	s_waitcnt lgkmcnt(0)
	buffer_store_dwordx4 v[252:255], v249, s[8:11], s100 offen sc1
	s_nop 1
	v_mbcnt_lo_u32_b32 v252, -1, 0
	v_mbcnt_hi_u32_b32 v252, -1, v252
	v_lshl_add_u32 v252, v252, 4, s99
	ds_read_b128 v[252:255], v252 offset:2048
	s_mov_b32 s100, 0x18000
	s_waitcnt lgkmcnt(0)
	buffer_store_dwordx4 v[252:255], v249, s[8:11], s100 offen sc1
	s_nop 1
	v_mbcnt_lo_u32_b32 v252, -1, 0
	v_mbcnt_hi_u32_b32 v252, -1, v252
	v_lshl_add_u32 v252, v252, 4, s99
	ds_read_b128 v[252:255], v252 offset:3072
	s_mov_b32 s100, 0x1c000
	s_waitcnt lgkmcnt(0)
	buffer_store_dwordx4 v[252:255], v249, s[8:11], s100 offen sc1
	s_nop 1
	s_waitcnt lgkmcnt(0)
	s_waitcnt vmcnt(0)
	s_waitcnt vmcnt(63) expcnt(7) lgkmcnt(15)
	s_barrier
	s_and_saveexec_b64 s[4:5], s[2:3]
	s_cbranch_execz .LBB0_1351
	s_mov_b64 s[8:9], exec
	v_mbcnt_lo_u32_b32 v0, s8, 0
	v_mbcnt_hi_u32_b32 v0, s9, v0
	v_cmp_eq_u32_e32 vcc, 0, v0
	s_and_b64 s[18:19], exec, vcc
	s_mov_b64 exec, s[18:19]
	s_cbranch_execz .LBB0_1351
	s_lshl_b32 s17, s35, 2
	s_lshl_b32 s16, s16, 9
	s_and_b32 s17, s17, 0x1f0
	s_or_b32 s16, s16, s17
	s_addk_i32 s16, 0xc00
	s_ashr_i32 s17, s16, 31
	s_lshl_b64 s[16:17], s[16:17], 2
	s_add_u32 s16, s25, s16
	s_addc_u32 s17, s26, s17
	s_bcnt1_i32_b64 s8, s[8:9]
	v_mov_b32_e32 v0, s8
	global_atomic_add v1, v0, s[16:17]
	s_branch .LBB0_1351

.LBB0_1606:
	v_mov_b32_e32 v128, 0
	s_add_u32 s0, s0, 0x3000000
	s_addc_u32 s1, s1, 0
	s_lshl_b32 s2, s8, 8
	v_mbcnt_lo_u32_b32 v128, -1, v128
	v_mbcnt_hi_u32_b32 v128, -1, v128
	s_add_i32 s19, s19, s2
	v_and_or_b32 v130, v128, 15, s19
	v_ashrrev_i32_e32 v128, 1, v128
	v_and_b32_e32 v128, -8, v128
	v_add_u32_e32 v128, s21, v128
	s_mov_b32 s3, 0
	s_lshl_b32 s2, s33, 8
	v_ashrrev_i32_e32 v129, 31, v128
	v_ashrrev_i32_e32 v131, 31, v130
	v_lshl_add_u64 v[132:133], v[128:129], 0, s[2:3]
	v_lshlrev_b64 v[128:129], 10, v[130:131]
	v_lshl_add_u64 v[128:129], v[132:133], 0, v[128:129]
	v_lshl_add_u64 v[142:143], v[128:129], 2, s[6:7]
	s_mov_b32 s3, 0x20000
	s_brev_b32 s2, 64
	s_and_b32 s1, s1, 0xffff
	v_lshlrev_b32_e32 v240, 1, v128
	v_lshl_add_u64 v[140:141], v[128:129], 2, s[6:7]
	global_load_dwordx4 v[144:147], v[140:141], off
	global_load_dwordx4 v[148:151], v[140:141], off offset:16
	global_load_dwordx4 v[152:155], v[140:141], off offset:512
	global_load_dwordx4 v[156:159], v[140:141], off offset:528
	s_mov_b64 s[10:11], 0x4000
	v_lshl_add_u64 v[138:139], v[128:129], 0, s[10:11]
	v_lshlrev_b32_e32 v241, 1, v138
	v_lshl_add_u64 v[140:141], v[138:139], 2, s[6:7]
	global_load_dwordx4 v[160:163], v[140:141], off
	global_load_dwordx4 v[164:167], v[140:141], off offset:16
	global_load_dwordx4 v[168:171], v[140:141], off offset:512
	global_load_dwordx4 v[172:175], v[140:141], off offset:528
	s_mov_b64 s[10:11], 0x8000
	v_lshl_add_u64 v[138:139], v[128:129], 0, s[10:11]
	v_lshlrev_b32_e32 v242, 1, v138
	v_lshl_add_u64 v[140:141], v[138:139], 2, s[6:7]
	global_load_dwordx4 v[176:179], v[140:141], off
	global_load_dwordx4 v[180:183], v[140:141], off offset:16
	global_load_dwordx4 v[184:187], v[140:141], off offset:512
	global_load_dwordx4 v[188:191], v[140:141], off offset:528
	s_mov_b64 s[10:11], 0xc000
	v_lshl_add_u64 v[138:139], v[128:129], 0, s[10:11]
	v_lshlrev_b32_e32 v243, 1, v138
	v_lshl_add_u64 v[140:141], v[138:139], 2, s[6:7]
	global_load_dwordx4 v[192:195], v[140:141], off
	global_load_dwordx4 v[196:199], v[140:141], off offset:16
	global_load_dwordx4 v[200:203], v[140:141], off offset:512
	global_load_dwordx4 v[204:207], v[140:141], off offset:528
	s_mov_b64 s[10:11], 0x20000
	v_lshl_add_u64 v[138:139], v[128:129], 0, s[10:11]
	v_lshlrev_b32_e32 v244, 1, v138
	v_lshl_add_u64 v[140:141], v[138:139], 2, s[6:7]
	global_load_dwordx4 v[208:211], v[140:141], off
	global_load_dwordx4 v[212:215], v[140:141], off offset:16
	global_load_dwordx4 v[216:219], v[140:141], off offset:512
	global_load_dwordx4 v[220:223], v[140:141], off offset:528
	s_mov_b64 s[10:11], 0x24000
	v_lshl_add_u64 v[138:139], v[128:129], 0, s[10:11]
	v_lshlrev_b32_e32 v245, 1, v138
	v_lshl_add_u64 v[140:141], v[138:139], 2, s[6:7]
	global_load_dwordx4 v[224:227], v[140:141], off
	global_load_dwordx4 v[228:231], v[140:141], off offset:16
	global_load_dwordx4 v[232:235], v[140:141], off offset:512
	global_load_dwordx4 v[236:239], v[140:141], off offset:528
	s_waitcnt vmcnt(22)
	v_add_f32_e32 v124, v124, v144
	v_add_f32_e32 v125, v125, v145
	v_add_f32_e32 v126, v126, v146
	v_add_f32_e32 v127, v127, v147
	v_add_f32_e32 v134, v122, v150
	v_add_f32_e32 v135, v123, v151
	v_add_f32_e32 v122, v120, v148
	v_add_f32_e32 v123, v121, v149
	v_cvt_pk_bf16_f32 v120, v124, v125
	v_cvt_pk_bf16_f32 v121, v126, v127
	v_cvt_pk_bf16_f32 v122, v122, v123
	v_cvt_pk_bf16_f32 v123, v134, v135
	buffer_store_dwordx4 v[120:123], v240, s[0:3], 0 offen sc1
	s_waitcnt vmcnt(21)
	v_add_f32_e32 v116, v116, v152
	v_add_f32_e32 v117, v117, v153
	v_add_f32_e32 v118, v118, v154
	v_add_f32_e32 v119, v119, v155
	v_add_f32_e32 v134, v114, v158
	v_add_f32_e32 v135, v115, v159
	v_add_f32_e32 v114, v112, v156
	v_add_f32_e32 v115, v113, v157
	v_cvt_pk_bf16_f32 v112, v116, v117
	v_cvt_pk_bf16_f32 v113, v118, v119
	v_cvt_pk_bf16_f32 v114, v114, v115
	v_cvt_pk_bf16_f32 v115, v134, v135
	buffer_store_dwordx4 v[112:115], v240, s[0:3], 0 offen offset:256 sc1
	s_mov_b64 s[10:11], 0x28000
	v_lshl_add_u64 v[138:139], v[128:129], 0, s[10:11]
	v_lshlrev_b32_e32 v246, 1, v138
	v_lshl_add_u64 v[140:141], v[138:139], 2, s[6:7]
	global_load_dwordx4 v[144:147], v[140:141], off
	global_load_dwordx4 v[148:151], v[140:141], off offset:16
	global_load_dwordx4 v[152:155], v[140:141], off offset:512
	global_load_dwordx4 v[156:159], v[140:141], off offset:528
	s_waitcnt vmcnt(24)
	v_add_f32_e32 v108, v108, v160
	v_add_f32_e32 v109, v109, v161
	v_add_f32_e32 v110, v110, v162
	v_add_f32_e32 v111, v111, v163
	v_add_f32_e32 v134, v106, v166
	v_add_f32_e32 v135, v107, v167
	v_add_f32_e32 v106, v104, v164
	v_add_f32_e32 v107, v105, v165
	v_cvt_pk_bf16_f32 v104, v108, v109
	v_cvt_pk_bf16_f32 v105, v110, v111
	v_cvt_pk_bf16_f32 v106, v106, v107
	v_cvt_pk_bf16_f32 v107, v134, v135
	buffer_store_dwordx4 v[104:107], v241, s[0:3], 0 offen sc1
	s_waitcnt vmcnt(23)
	v_add_f32_e32 v100, v100, v168
	v_add_f32_e32 v101, v101, v169
	v_add_f32_e32 v102, v102, v170
	v_add_f32_e32 v103, v103, v171
	v_add_f32_e32 v134, v98, v174
	v_add_f32_e32 v135, v99, v175
	v_add_f32_e32 v98, v96, v172
	v_add_f32_e32 v99, v97, v173
	v_cvt_pk_bf16_f32 v96, v100, v101
	v_cvt_pk_bf16_f32 v97, v102, v103
	v_cvt_pk_bf16_f32 v98, v98, v99
	v_cvt_pk_bf16_f32 v99, v134, v135
	buffer_store_dwordx4 v[96:99], v241, s[0:3], 0 offen offset:256 sc1
	s_mov_b64 s[10:11], 0x2c000
	v_lshl_add_u64 v[138:139], v[128:129], 0, s[10:11]
	v_lshlrev_b32_e32 v247, 1, v138
	v_lshl_add_u64 v[140:141], v[138:139], 2, s[6:7]
	global_load_dwordx4 v[160:163], v[140:141], off
	global_load_dwordx4 v[164:167], v[140:141], off offset:16
	global_load_dwordx4 v[168:171], v[140:141], off offset:512
	global_load_dwordx4 v[172:175], v[140:141], off offset:528
	s_waitcnt vmcnt(26)
	v_add_f32_e32 v92, v92, v176
	v_add_f32_e32 v93, v93, v177
	v_add_f32_e32 v94, v94, v178
	v_add_f32_e32 v95, v95, v179
	v_add_f32_e32 v134, v90, v182
	v_add_f32_e32 v135, v91, v183
	v_add_f32_e32 v90, v88, v180
	v_add_f32_e32 v91, v89, v181
	v_cvt_pk_bf16_f32 v88, v92, v93
	v_cvt_pk_bf16_f32 v89, v94, v95
	v_cvt_pk_bf16_f32 v90, v90, v91
	v_cvt_pk_bf16_f32 v91, v134, v135
	buffer_store_dwordx4 v[88:91], v242, s[0:3], 0 offen sc1
	s_waitcnt vmcnt(25)
	v_add_f32_e32 v84, v84, v184
	v_add_f32_e32 v85, v85, v185
	v_add_f32_e32 v86, v86, v186
	v_add_f32_e32 v87, v87, v187
	v_add_f32_e32 v134, v82, v190
	v_add_f32_e32 v135, v83, v191
	v_add_f32_e32 v82, v80, v188
	v_add_f32_e32 v83, v81, v189
	v_cvt_pk_bf16_f32 v80, v84, v85
	v_cvt_pk_bf16_f32 v81, v86, v87
	v_cvt_pk_bf16_f32 v82, v82, v83
	v_cvt_pk_bf16_f32 v83, v134, v135
	buffer_store_dwordx4 v[80:83], v242, s[0:3], 0 offen offset:256 sc1
	s_waitcnt vmcnt(24)
	v_add_f32_e32 v76, v76, v192
	v_add_f32_e32 v77, v77, v193
	v_add_f32_e32 v78, v78, v194
	v_add_f32_e32 v79, v79, v195
	v_add_f32_e32 v134, v74, v198
	v_add_f32_e32 v135, v75, v199
	v_add_f32_e32 v74, v72, v196
	v_add_f32_e32 v75, v73, v197
	v_cvt_pk_bf16_f32 v72, v76, v77
	v_cvt_pk_bf16_f32 v73, v78, v79
	v_cvt_pk_bf16_f32 v74, v74, v75
	v_cvt_pk_bf16_f32 v75, v134, v135
	buffer_store_dwordx4 v[72:75], v243, s[0:3], 0 offen sc1
	s_waitcnt vmcnt(23)
	v_add_f32_e32 v68, v68, v200
	v_add_f32_e32 v69, v69, v201
	v_add_f32_e32 v70, v70, v202
	v_add_f32_e32 v71, v71, v203
	v_add_f32_e32 v134, v66, v206
	v_add_f32_e32 v135, v67, v207
	v_add_f32_e32 v66, v64, v204
	v_add_f32_e32 v67, v65, v205
	v_cvt_pk_bf16_f32 v64, v68, v69
	v_cvt_pk_bf16_f32 v65, v70, v71
	v_cvt_pk_bf16_f32 v66, v66, v67
	v_cvt_pk_bf16_f32 v67, v134, v135
	buffer_store_dwordx4 v[64:67], v243, s[0:3], 0 offen offset:256 sc1
	s_waitcnt vmcnt(22)
	v_add_f32_e32 v60, v60, v208
	v_add_f32_e32 v61, v61, v209
	v_add_f32_e32 v62, v62, v210
	v_add_f32_e32 v63, v63, v211
	v_add_f32_e32 v134, v58, v214
	v_add_f32_e32 v135, v59, v215
	v_add_f32_e32 v58, v56, v212
	v_add_f32_e32 v59, v57, v213
	v_cvt_pk_bf16_f32 v56, v60, v61
	v_cvt_pk_bf16_f32 v57, v62, v63
	v_cvt_pk_bf16_f32 v58, v58, v59
	v_cvt_pk_bf16_f32 v59, v134, v135
	buffer_store_dwordx4 v[56:59], v244, s[0:3], 0 offen sc1
	s_waitcnt vmcnt(21)
	v_add_f32_e32 v52, v52, v216
	v_add_f32_e32 v53, v53, v217
	v_add_f32_e32 v54, v54, v218
	v_add_f32_e32 v55, v55, v219
	v_add_f32_e32 v134, v50, v222
	v_add_f32_e32 v135, v51, v223
	v_add_f32_e32 v50, v48, v220
	v_add_f32_e32 v51, v49, v221
	v_cvt_pk_bf16_f32 v48, v52, v53
	v_cvt_pk_bf16_f32 v49, v54, v55
	v_cvt_pk_bf16_f32 v50, v50, v51
	v_cvt_pk_bf16_f32 v51, v134, v135
	buffer_store_dwordx4 v[48:51], v244, s[0:3], 0 offen offset:256 sc1
	s_waitcnt vmcnt(20)
	v_add_f32_e32 v44, v44, v224
	v_add_f32_e32 v45, v45, v225
	v_add_f32_e32 v46, v46, v226
	v_add_f32_e32 v47, v47, v227
	v_add_f32_e32 v134, v42, v230
	v_add_f32_e32 v135, v43, v231
	v_add_f32_e32 v42, v40, v228
	v_add_f32_e32 v43, v41, v229
	v_cvt_pk_bf16_f32 v40, v44, v45
	v_cvt_pk_bf16_f32 v41, v46, v47
	v_cvt_pk_bf16_f32 v42, v42, v43
	v_cvt_pk_bf16_f32 v43, v134, v135
	buffer_store_dwordx4 v[40:43], v245, s[0:3], 0 offen sc1
	s_waitcnt vmcnt(19)
	v_add_f32_e32 v36, v36, v232
	v_add_f32_e32 v37, v37, v233
	v_add_f32_e32 v38, v38, v234
	v_add_f32_e32 v39, v39, v235
	v_add_f32_e32 v134, v34, v238
	v_add_f32_e32 v135, v35, v239
	v_add_f32_e32 v34, v32, v236
	v_add_f32_e32 v35, v33, v237
	v_cvt_pk_bf16_f32 v32, v36, v37
	v_cvt_pk_bf16_f32 v33, v38, v39
	v_cvt_pk_bf16_f32 v34, v34, v35
	v_cvt_pk_bf16_f32 v35, v134, v135
	buffer_store_dwordx4 v[32:35], v245, s[0:3], 0 offen offset:256 sc1
	s_waitcnt vmcnt(16)
	v_add_f32_e32 v28, v28, v144
	v_add_f32_e32 v29, v29, v145
	v_add_f32_e32 v30, v30, v146
	v_add_f32_e32 v31, v31, v147
	v_add_f32_e32 v134, v26, v150
	v_add_f32_e32 v135, v27, v151
	v_add_f32_e32 v26, v24, v148
	v_add_f32_e32 v27, v25, v149
	v_cvt_pk_bf16_f32 v24, v28, v29
	v_cvt_pk_bf16_f32 v25, v30, v31
	v_cvt_pk_bf16_f32 v26, v26, v27
	v_cvt_pk_bf16_f32 v27, v134, v135
	buffer_store_dwordx4 v[24:27], v246, s[0:3], 0 offen sc1
	s_waitcnt vmcnt(15)
	v_add_f32_e32 v20, v20, v152
	v_add_f32_e32 v21, v21, v153
	v_add_f32_e32 v22, v22, v154
	v_add_f32_e32 v23, v23, v155
	v_add_f32_e32 v134, v18, v158
	v_add_f32_e32 v135, v19, v159
	v_add_f32_e32 v18, v16, v156
	v_add_f32_e32 v19, v17, v157
	v_cvt_pk_bf16_f32 v16, v20, v21
	v_cvt_pk_bf16_f32 v17, v22, v23
	v_cvt_pk_bf16_f32 v18, v18, v19
	v_cvt_pk_bf16_f32 v19, v134, v135
	buffer_store_dwordx4 v[16:19], v246, s[0:3], 0 offen offset:256 sc1
	s_waitcnt vmcnt(12)
	v_add_f32_e32 v12, v12, v160
	v_add_f32_e32 v13, v13, v161
	v_add_f32_e32 v14, v14, v162
	v_add_f32_e32 v15, v15, v163
	v_add_f32_e32 v134, v10, v166
	v_add_f32_e32 v135, v11, v167
	v_add_f32_e32 v10, v8, v164
	v_add_f32_e32 v11, v9, v165
	v_cvt_pk_bf16_f32 v8, v12, v13
	v_cvt_pk_bf16_f32 v9, v14, v15
	v_cvt_pk_bf16_f32 v10, v10, v11
	v_cvt_pk_bf16_f32 v11, v134, v135
	buffer_store_dwordx4 v[8:11], v247, s[0:3], 0 offen sc1
	s_waitcnt vmcnt(11)
	v_add_f32_e32 v4, v4, v168
	v_add_f32_e32 v5, v5, v169
	v_add_f32_e32 v6, v6, v170
	v_add_f32_e32 v7, v7, v171
	v_add_f32_e32 v134, v2, v174
	v_add_f32_e32 v135, v3, v175
	v_add_f32_e32 v2, v0, v172
	v_add_f32_e32 v3, v1, v173
	v_cvt_pk_bf16_f32 v0, v4, v5
	v_cvt_pk_bf16_f32 v1, v6, v7
	v_cvt_pk_bf16_f32 v2, v2, v3
	v_cvt_pk_bf16_f32 v3, v134, v135
	buffer_store_dwordx4 v[0:3], v247, s[0:3], 0 offen offset:256 sc1
	s_waitcnt vmcnt(0)
	s_barrier

	.amdhsa_kernel _Z6mk_fwd4Args
		.amdhsa_group_segment_fixed_size 0
		.amdhsa_private_segment_fixed_size 0
		.amdhsa_kernarg_size 448
		.amdhsa_user_sgpr_count 2
		.amdhsa_user_sgpr_dispatch_ptr 0
		.amdhsa_user_sgpr_queue_ptr 0
		.amdhsa_user_sgpr_kernarg_segment_ptr 1
		.amdhsa_user_sgpr_dispatch_id 0
		.amdhsa_user_sgpr_kernarg_preload_length 0
		.amdhsa_user_sgpr_kernarg_preload_offset 0
		.amdhsa_user_sgpr_private_segment_size 0
		.amdhsa_uses_dynamic_stack 0
		.amdhsa_enable_private_segment 0
		.amdhsa_system_sgpr_workgroup_id_x 1
		.amdhsa_system_sgpr_workgroup_id_y 0
		.amdhsa_system_sgpr_workgroup_id_z 0
		.amdhsa_system_sgpr_workgroup_info 0
		.amdhsa_system_vgpr_workitem_id 0
		.amdhsa_next_free_vgpr 256
		.amdhsa_next_free_sgpr 102
		.amdhsa_accum_offset 256
		.amdhsa_reserve_vcc 1
		.amdhsa_float_round_mode_32 0
		.amdhsa_float_round_mode_16_64 0
		.amdhsa_float_denorm_mode_32 3
		.amdhsa_float_denorm_mode_16_64 3
		.amdhsa_dx10_clamp 1
		.amdhsa_ieee_mode 1
		.amdhsa_fp16_overflow 0
		.amdhsa_tg_split 0
		.amdhsa_exception_fp_ieee_invalid_op 0
		.amdhsa_exception_fp_denorm_src 0
		.amdhsa_exception_fp_ieee_div_zero 0
		.amdhsa_exception_fp_ieee_overflow 0
		.amdhsa_exception_fp_ieee_underflow 0
		.amdhsa_exception_fp_ieee_inexact 0
		.amdhsa_exception_int_div_zero 0
	.end_amdhsa_kernel

amdhsa.kernels:
  - .agpr_count:     0
    .args:
      - .offset:         0
        .size:           192
        .value_kind:     by_value
      - .offset:         192
        .size:           4
        .value_kind:     hidden_block_count_x
      - .offset:         196
        .size:           4
        .value_kind:     hidden_block_count_y
      - .offset:         200
        .size:           4
        .value_kind:     hidden_block_count_z
      - .offset:         204
        .size:           2
        .value_kind:     hidden_group_size_x
      - .offset:         206
        .size:           2
        .value_kind:     hidden_group_size_y
      - .offset:         208
        .size:           2
        .value_kind:     hidden_group_size_z
      - .offset:         210
        .size:           2
        .value_kind:     hidden_remainder_x
      - .offset:         212
        .size:           2
        .value_kind:     hidden_remainder_y
      - .offset:         214
        .size:           2
        .value_kind:     hidden_remainder_z
      - .offset:         232
        .size:           8
        .value_kind:     hidden_global_offset_x
      - .offset:         240
        .size:           8
        .value_kind:     hidden_global_offset_y
      - .offset:         248
        .size:           8
        .value_kind:     hidden_global_offset_z
      - .offset:         256
        .size:           2
        .value_kind:     hidden_grid_dims
      - .offset:         312
        .size:           4
        .value_kind:     hidden_dynamic_lds_size
    .group_segment_fixed_size: 0
    .kernarg_segment_align: 8
    .kernarg_segment_size: 448
    .language:       OpenCL C
    .language_version:
      - 2
      - 0
    .max_flat_workgroup_size: 512
    .name:           _Z6mk_fwd4Args
    .private_segment_fixed_size: 0
    .sgpr_count:     108
    .sgpr_spill_count: 261
    .symbol:         _Z6mk_fwd4Args.kd
    .uniform_work_group_size: 1
    .uses_dynamic_stack: false
    .vgpr_count:     256
    .vgpr_spill_count: 0
    .wavefront_size: 64
